# P9 epilogue: per-block counted vmcnt waits on the conv loads, gate-branch loads issued as each block frees its registers
# speedup vs baseline: 1.0110x; 1.0011x over previous
; #define LAS __attribute__((address_space(3)))
;     __device__ __forceinline__ void operator()(Acc& acc, const Unit& u, int wr, int wc, int fr_, int fq_, LAS unsigned char* le, int wid, int lane, int&) const {
;         asm volatile("" : "+v"(lane));
;         const int fr = lane & 15, fq = lane >> 4;
;         const int row0 = u.pm * 256, chb = (u.pn >> 1) * 256 + (u.pn & 1) * 128, ch0 = chb + wc * 32 + fq * 4, tid = wid * 64 + lane;
;         size_t roff = (size_t)(row0 + wr * 64 + 4 * fr) * DM + ch0;
;         LAS float* X = (LAS float*)le;
;         LAS float* C0 = X + 1024;
;         u32x2 xpre[2][4][2];
; #pragma unroll
;         for (int ai = 0; ai < 2; ++ai)
; #pragma unroll
;             for (int m = 0; m < 4; ++m)
; #pragma unroll
;                 for (int n = 0; n < 2; ++n) xpre[ai][m][n] = *(const u32x2*)(xc + roff + (size_t)(ai * 128 + m) * DM + n * 16);
;         float EA[2][2][4], EH[2][2][4];
; #pragma unroll
;         for (int ai = 0; ai < 2; ++ai) {
; #pragma unroll
;             for (int m = 0; m < 4; ++m) {
; #pragma unroll
;                 for (int n = 0; n < 2; ++n) {
;                     const f32x4 ba = *(const f32x4*)(b_a + ch0 + n * 16), bi = *(const f32x4*)(b_i + ch0 + n * 16), sl = *(const f32x4*)(spl + ch0 + n * 16);
;                     const u32x2 xw = xpre[ai][m][n]; const float xv[4] = {bflo(xw.x), bfhi(xw.x), bflo(xw.y), bfhi(xw.y)};
;                     const f32x4 ra = acc[ai][0][m][n] + ba, ri = acc[ai][1][m][n] + bi;
; #pragma unroll
;                     for (int j = 0; j < 4; ++j) { const float r = fast_sigmoid(ra[j]), ig = fast_sigmoid(ri[j]);
;                         const float la = -8.0f * r * sl[j];
;                         const float a = fast_exp(la); const float x2 = 2.0f * la;
;                         const float ser = -x2 * (1.0f + x2 * (0.5f + x2 * (1.0f / 6.0f + x2 * (1.0f / 24.0f + x2 * (1.0f / 120.0f)))));
;                         const float om = (x2 > -0.3f) ? ser : (1.0f - a * a);
;                         const float uu = __builtin_amdgcn_sqrtf(om) * (ig * xv[j]);
;                         if (m == 0) { acc[ai][0][m][n][j] = a; acc[ai][1][m][n][j] = uu; }
;                         else { acc[ai][1][m][n][j] = a * acc[ai][1][m - 1][n][j] + uu; acc[ai][0][m][n][j] = acc[ai][0][m - 1][n][j] * a; } } } }
.LBB0_1598:
	v_mbcnt_lo_u32_b32 v226, -1, 0
	v_mbcnt_hi_u32_b32 v226, -1, v226
	s_lshr_b32 s8, s91, 6
	s_lshr_b32 s9, s8, 2
	s_and_b32 s10, s8, 3
	v_and_b32_e32 v227, 15, v226
	v_lshrrev_b32_e32 v224, 4, v226
	v_add_u32_e32 v228, s91, v226
	s_lshl_b32 s11, s16, 7
	s_lshl_b32 s12, s10, 5
	s_add_i32 s12, s12, s11
	v_lshl_add_u32 v237, v224, 2, s12
	s_lshl_b32 s13, s18, 8
	s_lshl_b32 s15, s9, 6
	s_add_i32 s13, s13, s15
	v_lshl_add_u32 v238, v227, 2, s13
	v_lshl_add_u32 v238, v238, 11, v237
	v_lshlrev_b32_e32 v229, 1, v238
	v_add_u32_e32 v230, 0x1000, v229
	v_add_u32_e32 v231, 0x2000, v229
	v_add_u32_e32 v232, 0x3000, v229
	v_add_u32_e32 v233, 0x80000, v229
	v_add_u32_e32 v234, 0x81000, v229
	v_add_u32_e32 v235, 0x82000, v229
	v_add_u32_e32 v236, 0x83000, v229
	v_lshlrev_b32_e32 v239, 2, v237
	global_load_dwordx4 v[68:71], v239, s[42:43] offset:0
	global_load_dwordx4 v[100:103], v239, s[2:3] offset:0
	global_load_dwordx4 v[88:91], v239, s[44:45] offset:0
	global_load_dwordx4 v[72:75], v239, s[42:43] offset:64
	global_load_dwordx4 v[104:107], v239, s[2:3] offset:64
	global_load_dwordx4 v[198:201], v239, s[44:45] offset:64
	global_load_dwordx2 v[166:167], v229, s[40:41] offset:0
	global_load_dwordx2 v[168:169], v229, s[40:41] offset:32
	global_load_dwordx2 v[170:171], v230, s[40:41] offset:0
	global_load_dwordx2 v[172:173], v230, s[40:41] offset:32
	global_load_dwordx2 v[174:175], v231, s[40:41] offset:0
	global_load_dwordx2 v[176:177], v231, s[40:41] offset:32
	global_load_dwordx2 v[178:179], v232, s[40:41] offset:0
	global_load_dwordx2 v[180:181], v232, s[40:41] offset:32
	global_load_dwordx2 v[182:183], v233, s[40:41] offset:0
	global_load_dwordx2 v[184:185], v233, s[40:41] offset:32
	global_load_dwordx2 v[186:187], v234, s[40:41] offset:0
	global_load_dwordx2 v[188:189], v234, s[40:41] offset:32
	global_load_dwordx2 v[190:191], v235, s[40:41] offset:0
	global_load_dwordx2 v[192:193], v235, s[40:41] offset:32
	global_load_dwordx2 v[194:195], v236, s[40:41] offset:0
	global_load_dwordx2 v[196:197], v236, s[40:41] offset:32
	v_mov_b32_e32 v246, 0xbfb8aa3b
	v_mov_b32_e32 v247, 0x3fb8aa3b
	v_mov_b32_e32 v248, 1.0
	v_mov_b32_e32 v249, 0x3c088889
	v_mov_b32_e32 v250, 0x3d2aaaab
	v_mov_b32_e32 v251, 0x3e2aaaab
	v_mov_b32_e32 v252, 0.5
	v_mov_b32_e32 v253, 0xbe99999a
	s_mov_b32 s22, 0xffff0000
	s_waitcnt vmcnt(16)
	v_mul_f32_e32 v88, 0xc1000000, v88
	v_mul_f32_e32 v89, 0xc1000000, v89
	v_mul_f32_e32 v90, 0xc1000000, v90
	v_mul_f32_e32 v91, 0xc1000000, v91
	v_mul_f32_e32 v198, 0xc1000000, v198
	v_mul_f32_e32 v199, 0xc1000000, v199
	v_mul_f32_e32 v200, 0xc1000000, v200
	v_mul_f32_e32 v201, 0xc1000000, v201
	v_pk_add_f32 v[202:203], v[148:149], v[68:69] op_sel:[0,0] op_sel_hi:[1,1]
	v_pk_add_f32 v[204:205], v[150:151], v[70:71] op_sel:[0,0] op_sel_hi:[1,1]
	v_pk_add_f32 v[206:207], v[132:133], v[100:101] op_sel:[0,0] op_sel_hi:[1,1]
	v_pk_add_f32 v[208:209], v[134:135], v[102:103] op_sel:[0,0] op_sel_hi:[1,1]
	v_pk_mul_f32 v[202:203], v[202:203], v[246:247] op_sel:[0,0] op_sel_hi:[1,0]
	v_pk_mul_f32 v[204:205], v[204:205], v[246:247] op_sel:[0,0] op_sel_hi:[1,0]
	v_pk_mul_f32 v[206:207], v[206:207], v[246:247] op_sel:[0,0] op_sel_hi:[1,0]
	v_pk_mul_f32 v[208:209], v[208:209], v[246:247] op_sel:[0,0] op_sel_hi:[1,0]
	v_exp_f32_e32 v202, v202
	v_exp_f32_e32 v203, v203
	v_exp_f32_e32 v204, v204
	v_exp_f32_e32 v205, v205
	v_exp_f32_e32 v206, v206
	v_exp_f32_e32 v207, v207
	v_exp_f32_e32 v208, v208
	v_exp_f32_e32 v209, v209
	v_pk_add_f32 v[202:203], v[202:203], v[248:249] op_sel:[0,0] op_sel_hi:[1,0]
	v_pk_add_f32 v[204:205], v[204:205], v[248:249] op_sel:[0,0] op_sel_hi:[1,0]
	v_pk_add_f32 v[206:207], v[206:207], v[248:249] op_sel:[0,0] op_sel_hi:[1,0]
	v_pk_add_f32 v[208:209], v[208:209], v[248:249] op_sel:[0,0] op_sel_hi:[1,0]
	v_rcp_f32_e32 v202, v202
	v_rcp_f32_e32 v203, v203
	v_rcp_f32_e32 v204, v204
	v_rcp_f32_e32 v205, v205
	v_rcp_f32_e32 v206, v206
	v_rcp_f32_e32 v207, v207
	v_rcp_f32_e32 v208, v208
	v_rcp_f32_e32 v209, v209
	s_waitcnt vmcnt(15)
	v_lshlrev_b32_e32 v242, 16, v166
	v_and_b32_e32 v243, s22, v166
	v_lshlrev_b32_e32 v244, 16, v167
	v_and_b32_e32 v245, s22, v167
	global_load_dwordx2 v[166:167], v229, s[46:47] offset:0
	v_pk_mul_f32 v[210:211], v[202:203], v[88:89] op_sel:[0,0] op_sel_hi:[1,1]
	v_pk_mul_f32 v[212:213], v[204:205], v[90:91] op_sel:[0,0] op_sel_hi:[1,1]
	v_pk_mul_f32 v[206:207], v[206:207], v[242:243] op_sel:[0,0] op_sel_hi:[1,1]
	v_pk_mul_f32 v[208:209], v[208:209], v[244:245] op_sel:[0,0] op_sel_hi:[1,1]
	v_pk_mul_f32 v[214:215], v[210:211], v[246:247] op_sel:[0,1] op_sel_hi:[1,1]
	v_pk_mul_f32 v[216:217], v[212:213], v[246:247] op_sel:[0,1] op_sel_hi:[1,1]
	v_pk_add_f32 v[210:211], v[210:211], v[210:211] op_sel:[0,0] op_sel_hi:[1,1]
	v_pk_add_f32 v[212:213], v[212:213], v[212:213] op_sel:[0,0] op_sel_hi:[1,1]
	v_exp_f32_e32 v148, v214
	v_exp_f32_e32 v149, v215
	v_exp_f32_e32 v150, v216
	v_exp_f32_e32 v151, v217
	v_pk_fma_f32 v[238:239], v[210:211], v[248:249], v[250:251] op_sel:[0,1,0] op_sel_hi:[1,1,0]
	v_pk_fma_f32 v[240:241], v[212:213], v[248:249], v[250:251] op_sel:[0,1,0] op_sel_hi:[1,1,0]
	v_pk_fma_f32 v[238:239], v[210:211], v[238:239], v[250:251] op_sel:[0,0,1] op_sel_hi:[1,1,1]
	v_pk_fma_f32 v[240:241], v[212:213], v[240:241], v[250:251] op_sel:[0,0,1] op_sel_hi:[1,1,1]
	v_pk_fma_f32 v[238:239], v[210:211], v[238:239], v[252:253] op_sel:[0,0,0] op_sel_hi:[1,1,0]
	v_pk_fma_f32 v[240:241], v[212:213], v[240:241], v[252:253] op_sel:[0,0,0] op_sel_hi:[1,1,0]
	v_pk_fma_f32 v[238:239], v[210:211], v[238:239], v[248:249] op_sel:[0,0,0] op_sel_hi:[1,1,0]
	v_pk_fma_f32 v[240:241], v[212:213], v[240:241], v[248:249] op_sel:[0,0,0] op_sel_hi:[1,1,0]
; __device__ __forceinline__ float fast_exp(float x) { return __builtin_amdgcn_exp2f(x * 1.4426950408889634f); }
; __device__ __forceinline__ float fast_sigmoid(float x) { return __builtin_amdgcn_rcpf(1.0f + fast_exp(-x)); }
;     __device__ __forceinline__ void operator()(Acc& acc, const Unit& u, int wr, int wc, int fr_, int fq_, LAS unsigned char* le, int wid, int lane, int&) const {
;     ...
;                     const f32x4 ba = *(const f32x4*)(b_a + ch0 + n * 16), bi = *(const f32x4*)(b_i + ch0 + n * 16), sl = *(const f32x4*)(spl + ch0 + n * 16);
;                     const u32x2 xw = xpre[ai][m][n]; const float xv[4] = {bflo(xw.x), bfhi(xw.x), bflo(xw.y), bfhi(xw.y)};
;                     const f32x4 ra = acc[ai][0][m][n] + ba, ri = acc[ai][1][m][n] + bi;
; #pragma unroll
;                     for (int j = 0; j < 4; ++j) { const float r = fast_sigmoid(ra[j]), ig = fast_sigmoid(ri[j]);
;                         const float la = -8.0f * r * sl[j];
;                         const float a = fast_exp(la); const float x2 = 2.0f * la;
;                         const float ser = -x2 * (1.0f + x2 * (0.5f + x2 * (1.0f / 6.0f + x2 * (1.0f / 24.0f + x2 * (1.0f / 120.0f)))));
;                         const float om = (x2 > -0.3f) ? ser : (1.0f - a * a);
;                         const float uu = __builtin_amdgcn_sqrtf(om) * (ig * xv[j]);
;                         if (m == 0) { acc[ai][0][m][n][j] = a; acc[ai][1][m][n][j] = uu; }
;                         else { acc[ai][1][m][n][j] = a * acc[ai][1][m - 1][n][j] + uu; acc[ai][0][m][n][j] = acc[ai][0][m - 1][n][j] * a; } } } }
	v_pk_mul_f32 v[238:239], v[210:211], v[238:239] op_sel:[0,0] op_sel_hi:[1,1] neg_lo:[1,0] neg_hi:[1,0]
	v_pk_mul_f32 v[240:241], v[212:213], v[240:241] op_sel:[0,0] op_sel_hi:[1,1] neg_lo:[1,0] neg_hi:[1,0]
	v_pk_fma_f32 v[242:243], v[148:149], v[148:149], v[248:249] op_sel:[0,0,0] op_sel_hi:[1,1,0] neg_lo:[1,0,0] neg_hi:[1,0,0]
	v_pk_fma_f32 v[244:245], v[150:151], v[150:151], v[248:249] op_sel:[0,0,0] op_sel_hi:[1,1,0] neg_lo:[1,0,0] neg_hi:[1,0,0]
	v_cmp_lt_f32_e64 s[24:25], v253, v210
	v_cmp_lt_f32_e64 s[26:27], v253, v211
	v_cmp_lt_f32_e64 s[30:31], v253, v212
	v_cmp_lt_f32_e64 s[34:35], v253, v213
	v_cndmask_b32_e64 v238, v242, v238, s[24:25]
	v_cndmask_b32_e64 v239, v243, v239, s[26:27]
	v_cndmask_b32_e64 v240, v244, v240, s[30:31]
	v_cndmask_b32_e64 v241, v245, v241, s[34:35]
	v_sqrt_f32_e32 v238, v238
	v_sqrt_f32_e32 v239, v239
	v_sqrt_f32_e32 v240, v240
	v_sqrt_f32_e32 v241, v241
	v_pk_mul_f32 v[132:133], v[238:239], v[206:207] op_sel:[0,0] op_sel_hi:[1,1]
	v_pk_mul_f32 v[134:135], v[240:241], v[208:209] op_sel:[0,0] op_sel_hi:[1,1]
	v_pk_add_f32 v[202:203], v[116:117], v[72:73] op_sel:[0,0] op_sel_hi:[1,1]
	v_pk_add_f32 v[204:205], v[118:119], v[74:75] op_sel:[0,0] op_sel_hi:[1,1]
	v_pk_add_f32 v[206:207], v[92:93], v[104:105] op_sel:[0,0] op_sel_hi:[1,1]
	v_pk_add_f32 v[208:209], v[94:95], v[106:107] op_sel:[0,0] op_sel_hi:[1,1]
	v_pk_mul_f32 v[202:203], v[202:203], v[246:247] op_sel:[0,0] op_sel_hi:[1,0]
	v_pk_mul_f32 v[204:205], v[204:205], v[246:247] op_sel:[0,0] op_sel_hi:[1,0]
	v_pk_mul_f32 v[206:207], v[206:207], v[246:247] op_sel:[0,0] op_sel_hi:[1,0]
	v_pk_mul_f32 v[208:209], v[208:209], v[246:247] op_sel:[0,0] op_sel_hi:[1,0]
	v_exp_f32_e32 v202, v202
	v_exp_f32_e32 v203, v203
	v_exp_f32_e32 v204, v204
	v_exp_f32_e32 v205, v205
	v_exp_f32_e32 v206, v206
	v_exp_f32_e32 v207, v207
	v_exp_f32_e32 v208, v208
	v_exp_f32_e32 v209, v209
	v_pk_add_f32 v[202:203], v[202:203], v[248:249] op_sel:[0,0] op_sel_hi:[1,0]
	v_pk_add_f32 v[204:205], v[204:205], v[248:249] op_sel:[0,0] op_sel_hi:[1,0]
	v_pk_add_f32 v[206:207], v[206:207], v[248:249] op_sel:[0,0] op_sel_hi:[1,0]
	v_pk_add_f32 v[208:209], v[208:209], v[248:249] op_sel:[0,0] op_sel_hi:[1,0]
	v_rcp_f32_e32 v202, v202
	v_rcp_f32_e32 v203, v203
	v_rcp_f32_e32 v204, v204
	v_rcp_f32_e32 v205, v205
	v_rcp_f32_e32 v206, v206
	v_rcp_f32_e32 v207, v207
	v_rcp_f32_e32 v208, v208
	v_rcp_f32_e32 v209, v209
	s_waitcnt vmcnt(15)
	v_lshlrev_b32_e32 v242, 16, v168
	v_and_b32_e32 v243, s22, v168
	v_lshlrev_b32_e32 v244, 16, v169
	v_and_b32_e32 v245, s22, v169
	global_load_dwordx2 v[168:169], v229, s[46:47] offset:32
	v_pk_mul_f32 v[210:211], v[202:203], v[198:199] op_sel:[0,0] op_sel_hi:[1,1]
	v_pk_mul_f32 v[212:213], v[204:205], v[200:201] op_sel:[0,0] op_sel_hi:[1,1]
	v_pk_mul_f32 v[206:207], v[206:207], v[242:243] op_sel:[0,0] op_sel_hi:[1,1]
	v_pk_mul_f32 v[208:209], v[208:209], v[244:245] op_sel:[0,0] op_sel_hi:[1,1]
	v_pk_mul_f32 v[214:215], v[210:211], v[246:247] op_sel:[0,1] op_sel_hi:[1,1]
	v_pk_mul_f32 v[216:217], v[212:213], v[246:247] op_sel:[0,1] op_sel_hi:[1,1]
	v_pk_add_f32 v[210:211], v[210:211], v[210:211] op_sel:[0,0] op_sel_hi:[1,1]
	v_pk_add_f32 v[212:213], v[212:213], v[212:213] op_sel:[0,0] op_sel_hi:[1,1]
	v_exp_f32_e32 v116, v214
	v_exp_f32_e32 v117, v215
	v_exp_f32_e32 v118, v216
	v_exp_f32_e32 v119, v217
	v_pk_fma_f32 v[238:239], v[210:211], v[248:249], v[250:251] op_sel:[0,1,0] op_sel_hi:[1,1,0]
	v_pk_fma_f32 v[240:241], v[212:213], v[248:249], v[250:251] op_sel:[0,1,0] op_sel_hi:[1,1,0]
	v_pk_fma_f32 v[238:239], v[210:211], v[238:239], v[250:251] op_sel:[0,0,1] op_sel_hi:[1,1,1]
	v_pk_fma_f32 v[240:241], v[212:213], v[240:241], v[250:251] op_sel:[0,0,1] op_sel_hi:[1,1,1]
	v_pk_fma_f32 v[238:239], v[210:211], v[238:239], v[252:253] op_sel:[0,0,0] op_sel_hi:[1,1,0]
	v_pk_fma_f32 v[240:241], v[212:213], v[240:241], v[252:253] op_sel:[0,0,0] op_sel_hi:[1,1,0]
	v_pk_fma_f32 v[238:239], v[210:211], v[238:239], v[248:249] op_sel:[0,0,0] op_sel_hi:[1,1,0]
	v_pk_fma_f32 v[240:241], v[212:213], v[240:241], v[248:249] op_sel:[0,0,0] op_sel_hi:[1,1,0]
	v_pk_mul_f32 v[238:239], v[210:211], v[238:239] op_sel:[0,0] op_sel_hi:[1,1] neg_lo:[1,0] neg_hi:[1,0]
	v_pk_mul_f32 v[240:241], v[212:213], v[240:241] op_sel:[0,0] op_sel_hi:[1,1] neg_lo:[1,0] neg_hi:[1,0]
	v_pk_fma_f32 v[242:243], v[116:117], v[116:117], v[248:249] op_sel:[0,0,0] op_sel_hi:[1,1,0] neg_lo:[1,0,0] neg_hi:[1,0,0]
	v_pk_fma_f32 v[244:245], v[118:119], v[118:119], v[248:249] op_sel:[0,0,0] op_sel_hi:[1,1,0] neg_lo:[1,0,0] neg_hi:[1,0,0]
	v_cmp_lt_f32_e64 s[24:25], v253, v210
	v_cmp_lt_f32_e64 s[26:27], v253, v211
	v_cmp_lt_f32_e64 s[30:31], v253, v212
	v_cmp_lt_f32_e64 s[34:35], v253, v213
	v_cndmask_b32_e64 v238, v242, v238, s[24:25]
	v_cndmask_b32_e64 v239, v243, v239, s[26:27]
	v_cndmask_b32_e64 v240, v244, v240, s[30:31]
	v_cndmask_b32_e64 v241, v245, v241, s[34:35]
	v_sqrt_f32_e32 v238, v238
	v_sqrt_f32_e32 v239, v239
	v_sqrt_f32_e32 v240, v240
	v_sqrt_f32_e32 v241, v241
	v_pk_mul_f32 v[92:93], v[238:239], v[206:207] op_sel:[0,0] op_sel_hi:[1,1]
	v_pk_mul_f32 v[94:95], v[240:241], v[208:209] op_sel:[0,0] op_sel_hi:[1,1]
	v_pk_add_f32 v[202:203], v[144:145], v[68:69] op_sel:[0,0] op_sel_hi:[1,1]
	v_pk_add_f32 v[204:205], v[146:147], v[70:71] op_sel:[0,0] op_sel_hi:[1,1]
	v_pk_add_f32 v[206:207], v[128:129], v[100:101] op_sel:[0,0] op_sel_hi:[1,1]
	v_pk_add_f32 v[208:209], v[130:131], v[102:103] op_sel:[0,0] op_sel_hi:[1,1]
	v_pk_mul_f32 v[202:203], v[202:203], v[246:247] op_sel:[0,0] op_sel_hi:[1,0]
	v_pk_mul_f32 v[204:205], v[204:205], v[246:247] op_sel:[0,0] op_sel_hi:[1,0]
	v_pk_mul_f32 v[206:207], v[206:207], v[246:247] op_sel:[0,0] op_sel_hi:[1,0]
	v_pk_mul_f32 v[208:209], v[208:209], v[246:247] op_sel:[0,0] op_sel_hi:[1,0]
	v_exp_f32_e32 v202, v202
	v_exp_f32_e32 v203, v203
	v_exp_f32_e32 v204, v204
	v_exp_f32_e32 v205, v205
	v_exp_f32_e32 v206, v206
	v_exp_f32_e32 v207, v207
	v_exp_f32_e32 v208, v208
	v_exp_f32_e32 v209, v209
	v_pk_add_f32 v[202:203], v[202:203], v[248:249] op_sel:[0,0] op_sel_hi:[1,0]
	v_pk_add_f32 v[204:205], v[204:205], v[248:249] op_sel:[0,0] op_sel_hi:[1,0]
	v_pk_add_f32 v[206:207], v[206:207], v[248:249] op_sel:[0,0] op_sel_hi:[1,0]
	v_pk_add_f32 v[208:209], v[208:209], v[248:249] op_sel:[0,0] op_sel_hi:[1,0]
	v_rcp_f32_e32 v202, v202
	v_rcp_f32_e32 v203, v203
	v_rcp_f32_e32 v204, v204
	v_rcp_f32_e32 v205, v205
	v_rcp_f32_e32 v206, v206
	v_rcp_f32_e32 v207, v207
	v_rcp_f32_e32 v208, v208
	v_rcp_f32_e32 v209, v209
	s_waitcnt vmcnt(15)
; __device__ __forceinline__ float fast_exp(float x) { return __builtin_amdgcn_exp2f(x * 1.4426950408889634f); }
; __device__ __forceinline__ float fast_sigmoid(float x) { return __builtin_amdgcn_rcpf(1.0f + fast_exp(-x)); }
;     __device__ __forceinline__ void operator()(Acc& acc, const Unit& u, int wr, int wc, int fr_, int fq_, LAS unsigned char* le, int wid, int lane, int&) const {
;     ...
;                     const f32x4 ba = *(const f32x4*)(b_a + ch0 + n * 16), bi = *(const f32x4*)(b_i + ch0 + n * 16), sl = *(const f32x4*)(spl + ch0 + n * 16);
;                     const u32x2 xw = xpre[ai][m][n]; const float xv[4] = {bflo(xw.x), bfhi(xw.x), bflo(xw.y), bfhi(xw.y)};
;                     const f32x4 ra = acc[ai][0][m][n] + ba, ri = acc[ai][1][m][n] + bi;
; #pragma unroll
;                     for (int j = 0; j < 4; ++j) { const float r = fast_sigmoid(ra[j]), ig = fast_sigmoid(ri[j]);
;                         const float la = -8.0f * r * sl[j];
;                         const float a = fast_exp(la); const float x2 = 2.0f * la;
;                         const float ser = -x2 * (1.0f + x2 * (0.5f + x2 * (1.0f / 6.0f + x2 * (1.0f / 24.0f + x2 * (1.0f / 120.0f)))));
;                         const float om = (x2 > -0.3f) ? ser : (1.0f - a * a);
;                         const float uu = __builtin_amdgcn_sqrtf(om) * (ig * xv[j]);
;                         if (m == 0) { acc[ai][0][m][n][j] = a; acc[ai][1][m][n][j] = uu; }
;                         else { acc[ai][1][m][n][j] = a * acc[ai][1][m - 1][n][j] + uu; acc[ai][0][m][n][j] = acc[ai][0][m - 1][n][j] * a; } } } }
	v_lshlrev_b32_e32 v242, 16, v170
	v_and_b32_e32 v243, s22, v170
	v_lshlrev_b32_e32 v244, 16, v171
	v_and_b32_e32 v245, s22, v171
	global_load_dwordx2 v[170:171], v230, s[46:47] offset:0
	v_pk_mul_f32 v[210:211], v[202:203], v[88:89] op_sel:[0,0] op_sel_hi:[1,1]
	v_pk_mul_f32 v[212:213], v[204:205], v[90:91] op_sel:[0,0] op_sel_hi:[1,1]
	v_pk_mul_f32 v[206:207], v[206:207], v[242:243] op_sel:[0,0] op_sel_hi:[1,1]
	v_pk_mul_f32 v[208:209], v[208:209], v[244:245] op_sel:[0,0] op_sel_hi:[1,1]
	v_pk_mul_f32 v[214:215], v[210:211], v[246:247] op_sel:[0,1] op_sel_hi:[1,1]
	v_pk_mul_f32 v[216:217], v[212:213], v[246:247] op_sel:[0,1] op_sel_hi:[1,1]
	v_pk_add_f32 v[210:211], v[210:211], v[210:211] op_sel:[0,0] op_sel_hi:[1,1]
	v_pk_add_f32 v[212:213], v[212:213], v[212:213] op_sel:[0,0] op_sel_hi:[1,1]
	v_exp_f32_e32 v214, v214
	v_exp_f32_e32 v215, v215
	v_exp_f32_e32 v216, v216
	v_exp_f32_e32 v217, v217
	v_pk_fma_f32 v[238:239], v[210:211], v[248:249], v[250:251] op_sel:[0,1,0] op_sel_hi:[1,1,0]
	v_pk_fma_f32 v[240:241], v[212:213], v[248:249], v[250:251] op_sel:[0,1,0] op_sel_hi:[1,1,0]
	v_pk_fma_f32 v[238:239], v[210:211], v[238:239], v[250:251] op_sel:[0,0,1] op_sel_hi:[1,1,1]
	v_pk_fma_f32 v[240:241], v[212:213], v[240:241], v[250:251] op_sel:[0,0,1] op_sel_hi:[1,1,1]
	v_pk_fma_f32 v[238:239], v[210:211], v[238:239], v[252:253] op_sel:[0,0,0] op_sel_hi:[1,1,0]
	v_pk_fma_f32 v[240:241], v[212:213], v[240:241], v[252:253] op_sel:[0,0,0] op_sel_hi:[1,1,0]
	v_pk_fma_f32 v[238:239], v[210:211], v[238:239], v[248:249] op_sel:[0,0,0] op_sel_hi:[1,1,0]
	v_pk_fma_f32 v[240:241], v[212:213], v[240:241], v[248:249] op_sel:[0,0,0] op_sel_hi:[1,1,0]
	v_pk_mul_f32 v[238:239], v[210:211], v[238:239] op_sel:[0,0] op_sel_hi:[1,1] neg_lo:[1,0] neg_hi:[1,0]
	v_pk_mul_f32 v[240:241], v[212:213], v[240:241] op_sel:[0,0] op_sel_hi:[1,1] neg_lo:[1,0] neg_hi:[1,0]
	v_pk_fma_f32 v[242:243], v[214:215], v[214:215], v[248:249] op_sel:[0,0,0] op_sel_hi:[1,1,0] neg_lo:[1,0,0] neg_hi:[1,0,0]
	v_pk_fma_f32 v[244:245], v[216:217], v[216:217], v[248:249] op_sel:[0,0,0] op_sel_hi:[1,1,0] neg_lo:[1,0,0] neg_hi:[1,0,0]
	v_cmp_lt_f32_e64 s[24:25], v253, v210
	v_cmp_lt_f32_e64 s[26:27], v253, v211
	v_cmp_lt_f32_e64 s[30:31], v253, v212
	v_cmp_lt_f32_e64 s[34:35], v253, v213
	v_cndmask_b32_e64 v238, v242, v238, s[24:25]
	v_cndmask_b32_e64 v239, v243, v239, s[26:27]
	v_cndmask_b32_e64 v240, v244, v240, s[30:31]
	v_cndmask_b32_e64 v241, v245, v241, s[34:35]
	v_sqrt_f32_e32 v238, v238
	v_sqrt_f32_e32 v239, v239
	v_sqrt_f32_e32 v240, v240
	v_sqrt_f32_e32 v241, v241
	v_pk_mul_f32 v[206:207], v[238:239], v[206:207] op_sel:[0,0] op_sel_hi:[1,1]
	v_pk_mul_f32 v[208:209], v[240:241], v[208:209] op_sel:[0,0] op_sel_hi:[1,1]
	v_pk_fma_f32 v[128:129], v[214:215], v[132:133], v[206:207] op_sel:[0,0,0] op_sel_hi:[1,1,1]
	v_pk_fma_f32 v[130:131], v[216:217], v[134:135], v[208:209] op_sel:[0,0,0] op_sel_hi:[1,1,1]
	v_pk_mul_f32 v[144:145], v[148:149], v[214:215] op_sel:[0,0] op_sel_hi:[1,1]
	v_pk_mul_f32 v[146:147], v[150:151], v[216:217] op_sel:[0,0] op_sel_hi:[1,1]
	v_pk_add_f32 v[202:203], v[112:113], v[72:73] op_sel:[0,0] op_sel_hi:[1,1]
	v_pk_add_f32 v[204:205], v[114:115], v[74:75] op_sel:[0,0] op_sel_hi:[1,1]
	v_pk_add_f32 v[206:207], v[84:85], v[104:105] op_sel:[0,0] op_sel_hi:[1,1]
	v_pk_add_f32 v[208:209], v[86:87], v[106:107] op_sel:[0,0] op_sel_hi:[1,1]
	v_pk_mul_f32 v[202:203], v[202:203], v[246:247] op_sel:[0,0] op_sel_hi:[1,0]
	v_pk_mul_f32 v[204:205], v[204:205], v[246:247] op_sel:[0,0] op_sel_hi:[1,0]
	v_pk_mul_f32 v[206:207], v[206:207], v[246:247] op_sel:[0,0] op_sel_hi:[1,0]
	v_pk_mul_f32 v[208:209], v[208:209], v[246:247] op_sel:[0,0] op_sel_hi:[1,0]
	v_exp_f32_e32 v202, v202
	v_exp_f32_e32 v203, v203
	v_exp_f32_e32 v204, v204
	v_exp_f32_e32 v205, v205
	v_exp_f32_e32 v206, v206
	v_exp_f32_e32 v207, v207
	v_exp_f32_e32 v208, v208
	v_exp_f32_e32 v209, v209
	v_pk_add_f32 v[202:203], v[202:203], v[248:249] op_sel:[0,0] op_sel_hi:[1,0]
	v_pk_add_f32 v[204:205], v[204:205], v[248:249] op_sel:[0,0] op_sel_hi:[1,0]
	v_pk_add_f32 v[206:207], v[206:207], v[248:249] op_sel:[0,0] op_sel_hi:[1,0]
	v_pk_add_f32 v[208:209], v[208:209], v[248:249] op_sel:[0,0] op_sel_hi:[1,0]
	v_rcp_f32_e32 v202, v202
	v_rcp_f32_e32 v203, v203
	v_rcp_f32_e32 v204, v204
	v_rcp_f32_e32 v205, v205
	v_rcp_f32_e32 v206, v206
	v_rcp_f32_e32 v207, v207
	v_rcp_f32_e32 v208, v208
	v_rcp_f32_e32 v209, v209
	s_waitcnt vmcnt(15)
; __device__ __forceinline__ float fast_exp(float x) { return __builtin_amdgcn_exp2f(x * 1.4426950408889634f); }
; __device__ __forceinline__ float fast_sigmoid(float x) { return __builtin_amdgcn_rcpf(1.0f + fast_exp(-x)); }
;     __device__ __forceinline__ void operator()(Acc& acc, const Unit& u, int wr, int wc, int fr_, int fq_, LAS unsigned char* le, int wid, int lane, int&) const {
;     ...
;                 for (int n = 0; n < 2; ++n) {
;                     const f32x4 ba = *(const f32x4*)(b_a + ch0 + n * 16), bi = *(const f32x4*)(b_i + ch0 + n * 16), sl = *(const f32x4*)(spl + ch0 + n * 16);
;                     const u32x2 xw = xpre[ai][m][n]; const float xv[4] = {bflo(xw.x), bfhi(xw.x), bflo(xw.y), bfhi(xw.y)};
;                     const f32x4 ra = acc[ai][0][m][n] + ba, ri = acc[ai][1][m][n] + bi;
; #pragma unroll
;                     for (int j = 0; j < 4; ++j) { const float r = fast_sigmoid(ra[j]), ig = fast_sigmoid(ri[j]);
;                         const float la = -8.0f * r * sl[j];
;                         const float a = fast_exp(la); const float x2 = 2.0f * la;
;                         const float ser = -x2 * (1.0f + x2 * (0.5f + x2 * (1.0f / 6.0f + x2 * (1.0f / 24.0f + x2 * (1.0f / 120.0f)))));
;                         const float om = (x2 > -0.3f) ? ser : (1.0f - a * a);
;                         const float uu = __builtin_amdgcn_sqrtf(om) * (ig * xv[j]);
;                         if (m == 0) { acc[ai][0][m][n][j] = a; acc[ai][1][m][n][j] = uu; }
;                         else { acc[ai][1][m][n][j] = a * acc[ai][1][m - 1][n][j] + uu; acc[ai][0][m][n][j] = acc[ai][0][m - 1][n][j] * a; } } } }
;     ...
;         u32x2 gpre[2][4][2];
; #pragma unroll
;         for (int m = 0; m < 4; ++m)
; #pragma unroll
;             for (int n = 0; n < 2; ++n) gpre[0][m][n] = *(const u32x2*)(gg + roff + (size_t)m * DM + n * 16);
	v_lshlrev_b32_e32 v242, 16, v172
	v_and_b32_e32 v243, s22, v172
	v_lshlrev_b32_e32 v244, 16, v173
	v_and_b32_e32 v245, s22, v173
	global_load_dwordx2 v[172:173], v230, s[46:47] offset:32
	v_pk_mul_f32 v[210:211], v[202:203], v[198:199] op_sel:[0,0] op_sel_hi:[1,1]
	v_pk_mul_f32 v[212:213], v[204:205], v[200:201] op_sel:[0,0] op_sel_hi:[1,1]
	v_pk_mul_f32 v[206:207], v[206:207], v[242:243] op_sel:[0,0] op_sel_hi:[1,1]
	v_pk_mul_f32 v[208:209], v[208:209], v[244:245] op_sel:[0,0] op_sel_hi:[1,1]
	v_pk_mul_f32 v[214:215], v[210:211], v[246:247] op_sel:[0,1] op_sel_hi:[1,1]
	v_pk_mul_f32 v[216:217], v[212:213], v[246:247] op_sel:[0,1] op_sel_hi:[1,1]
	v_pk_add_f32 v[210:211], v[210:211], v[210:211] op_sel:[0,0] op_sel_hi:[1,1]
	v_pk_add_f32 v[212:213], v[212:213], v[212:213] op_sel:[0,0] op_sel_hi:[1,1]
	v_exp_f32_e32 v214, v214
	v_exp_f32_e32 v215, v215
	v_exp_f32_e32 v216, v216
	v_exp_f32_e32 v217, v217
	v_pk_fma_f32 v[238:239], v[210:211], v[248:249], v[250:251] op_sel:[0,1,0] op_sel_hi:[1,1,0]
	v_pk_fma_f32 v[240:241], v[212:213], v[248:249], v[250:251] op_sel:[0,1,0] op_sel_hi:[1,1,0]
	v_pk_fma_f32 v[238:239], v[210:211], v[238:239], v[250:251] op_sel:[0,0,1] op_sel_hi:[1,1,1]
	v_pk_fma_f32 v[240:241], v[212:213], v[240:241], v[250:251] op_sel:[0,0,1] op_sel_hi:[1,1,1]
	v_pk_fma_f32 v[238:239], v[210:211], v[238:239], v[252:253] op_sel:[0,0,0] op_sel_hi:[1,1,0]
	v_pk_fma_f32 v[240:241], v[212:213], v[240:241], v[252:253] op_sel:[0,0,0] op_sel_hi:[1,1,0]
	v_pk_fma_f32 v[238:239], v[210:211], v[238:239], v[248:249] op_sel:[0,0,0] op_sel_hi:[1,1,0]
	v_pk_fma_f32 v[240:241], v[212:213], v[240:241], v[248:249] op_sel:[0,0,0] op_sel_hi:[1,1,0]
	v_pk_mul_f32 v[238:239], v[210:211], v[238:239] op_sel:[0,0] op_sel_hi:[1,1] neg_lo:[1,0] neg_hi:[1,0]
	v_pk_mul_f32 v[240:241], v[212:213], v[240:241] op_sel:[0,0] op_sel_hi:[1,1] neg_lo:[1,0] neg_hi:[1,0]
	v_pk_fma_f32 v[242:243], v[214:215], v[214:215], v[248:249] op_sel:[0,0,0] op_sel_hi:[1,1,0] neg_lo:[1,0,0] neg_hi:[1,0,0]
	v_pk_fma_f32 v[244:245], v[216:217], v[216:217], v[248:249] op_sel:[0,0,0] op_sel_hi:[1,1,0] neg_lo:[1,0,0] neg_hi:[1,0,0]
	v_cmp_lt_f32_e64 s[24:25], v253, v210
	v_cmp_lt_f32_e64 s[26:27], v253, v211
	v_cmp_lt_f32_e64 s[30:31], v253, v212
	v_cmp_lt_f32_e64 s[34:35], v253, v213
	v_cndmask_b32_e64 v238, v242, v238, s[24:25]
	v_cndmask_b32_e64 v239, v243, v239, s[26:27]
	v_cndmask_b32_e64 v240, v244, v240, s[30:31]
	v_cndmask_b32_e64 v241, v245, v241, s[34:35]
	v_sqrt_f32_e32 v238, v238
	v_sqrt_f32_e32 v239, v239
	v_sqrt_f32_e32 v240, v240
	v_sqrt_f32_e32 v241, v241
	v_pk_mul_f32 v[206:207], v[238:239], v[206:207] op_sel:[0,0] op_sel_hi:[1,1]
	v_pk_mul_f32 v[208:209], v[240:241], v[208:209] op_sel:[0,0] op_sel_hi:[1,1]
	v_pk_fma_f32 v[84:85], v[214:215], v[92:93], v[206:207] op_sel:[0,0,0] op_sel_hi:[1,1,1]
	v_pk_fma_f32 v[86:87], v[216:217], v[94:95], v[208:209] op_sel:[0,0,0] op_sel_hi:[1,1,1]
	v_pk_mul_f32 v[112:113], v[116:117], v[214:215] op_sel:[0,0] op_sel_hi:[1,1]
	v_pk_mul_f32 v[114:115], v[118:119], v[216:217] op_sel:[0,0] op_sel_hi:[1,1]
	v_pk_add_f32 v[202:203], v[140:141], v[68:69] op_sel:[0,0] op_sel_hi:[1,1]
	v_pk_add_f32 v[204:205], v[142:143], v[70:71] op_sel:[0,0] op_sel_hi:[1,1]
	v_pk_add_f32 v[206:207], v[124:125], v[100:101] op_sel:[0,0] op_sel_hi:[1,1]
	v_pk_add_f32 v[208:209], v[126:127], v[102:103] op_sel:[0,0] op_sel_hi:[1,1]
	v_pk_mul_f32 v[202:203], v[202:203], v[246:247] op_sel:[0,0] op_sel_hi:[1,0]
	v_pk_mul_f32 v[204:205], v[204:205], v[246:247] op_sel:[0,0] op_sel_hi:[1,0]
	v_pk_mul_f32 v[206:207], v[206:207], v[246:247] op_sel:[0,0] op_sel_hi:[1,0]
	v_pk_mul_f32 v[208:209], v[208:209], v[246:247] op_sel:[0,0] op_sel_hi:[1,0]
	v_exp_f32_e32 v202, v202
	v_exp_f32_e32 v203, v203
	v_exp_f32_e32 v204, v204
	v_exp_f32_e32 v205, v205
	v_exp_f32_e32 v206, v206
	v_exp_f32_e32 v207, v207
	v_exp_f32_e32 v208, v208
	v_exp_f32_e32 v209, v209
	v_pk_add_f32 v[202:203], v[202:203], v[248:249] op_sel:[0,0] op_sel_hi:[1,0]
	v_pk_add_f32 v[204:205], v[204:205], v[248:249] op_sel:[0,0] op_sel_hi:[1,0]
	v_pk_add_f32 v[206:207], v[206:207], v[248:249] op_sel:[0,0] op_sel_hi:[1,0]
	v_pk_add_f32 v[208:209], v[208:209], v[248:249] op_sel:[0,0] op_sel_hi:[1,0]
	v_rcp_f32_e32 v202, v202
	v_rcp_f32_e32 v203, v203
	v_rcp_f32_e32 v204, v204
	v_rcp_f32_e32 v205, v205
	v_rcp_f32_e32 v206, v206
	v_rcp_f32_e32 v207, v207
	v_rcp_f32_e32 v208, v208
	v_rcp_f32_e32 v209, v209
	s_waitcnt vmcnt(15)
; __device__ __forceinline__ float fast_exp(float x) { return __builtin_amdgcn_exp2f(x * 1.4426950408889634f); }
; __device__ __forceinline__ float fast_sigmoid(float x) { return __builtin_amdgcn_rcpf(1.0f + fast_exp(-x)); }
;     __device__ __forceinline__ void operator()(Acc& acc, const Unit& u, int wr, int wc, int fr_, int fq_, LAS unsigned char* le, int wid, int lane, int&) const {
;     ...
;                 for (int n = 0; n < 2; ++n) {
;                     const f32x4 ba = *(const f32x4*)(b_a + ch0 + n * 16), bi = *(const f32x4*)(b_i + ch0 + n * 16), sl = *(const f32x4*)(spl + ch0 + n * 16);
;                     const u32x2 xw = xpre[ai][m][n]; const float xv[4] = {bflo(xw.x), bfhi(xw.x), bflo(xw.y), bfhi(xw.y)};
;                     const f32x4 ra = acc[ai][0][m][n] + ba, ri = acc[ai][1][m][n] + bi;
; #pragma unroll
;                     for (int j = 0; j < 4; ++j) { const float r = fast_sigmoid(ra[j]), ig = fast_sigmoid(ri[j]);
;                         const float la = -8.0f * r * sl[j];
;                         const float a = fast_exp(la); const float x2 = 2.0f * la;
;                         const float ser = -x2 * (1.0f + x2 * (0.5f + x2 * (1.0f / 6.0f + x2 * (1.0f / 24.0f + x2 * (1.0f / 120.0f)))));
;                         const float om = (x2 > -0.3f) ? ser : (1.0f - a * a);
;                         const float uu = __builtin_amdgcn_sqrtf(om) * (ig * xv[j]);
;                         if (m == 0) { acc[ai][0][m][n][j] = a; acc[ai][1][m][n][j] = uu; }
;                         else { acc[ai][1][m][n][j] = a * acc[ai][1][m - 1][n][j] + uu; acc[ai][0][m][n][j] = acc[ai][0][m - 1][n][j] * a; } } } }
;     ...
;         u32x2 gpre[2][4][2];
; #pragma unroll
;         for (int m = 0; m < 4; ++m)
; #pragma unroll
;             for (int n = 0; n < 2; ++n) gpre[0][m][n] = *(const u32x2*)(gg + roff + (size_t)m * DM + n * 16);
	v_lshlrev_b32_e32 v242, 16, v174
	v_and_b32_e32 v243, s22, v174
	v_lshlrev_b32_e32 v244, 16, v175
	v_and_b32_e32 v245, s22, v175
	global_load_dwordx2 v[174:175], v231, s[46:47] offset:0
	v_pk_mul_f32 v[210:211], v[202:203], v[88:89] op_sel:[0,0] op_sel_hi:[1,1]
	v_pk_mul_f32 v[212:213], v[204:205], v[90:91] op_sel:[0,0] op_sel_hi:[1,1]
	v_pk_mul_f32 v[206:207], v[206:207], v[242:243] op_sel:[0,0] op_sel_hi:[1,1]
	v_pk_mul_f32 v[208:209], v[208:209], v[244:245] op_sel:[0,0] op_sel_hi:[1,1]
	v_pk_mul_f32 v[214:215], v[210:211], v[246:247] op_sel:[0,1] op_sel_hi:[1,1]
	v_pk_mul_f32 v[216:217], v[212:213], v[246:247] op_sel:[0,1] op_sel_hi:[1,1]
	v_pk_add_f32 v[210:211], v[210:211], v[210:211] op_sel:[0,0] op_sel_hi:[1,1]
	v_pk_add_f32 v[212:213], v[212:213], v[212:213] op_sel:[0,0] op_sel_hi:[1,1]
	v_exp_f32_e32 v214, v214
	v_exp_f32_e32 v215, v215
	v_exp_f32_e32 v216, v216
	v_exp_f32_e32 v217, v217
	v_pk_fma_f32 v[238:239], v[210:211], v[248:249], v[250:251] op_sel:[0,1,0] op_sel_hi:[1,1,0]
	v_pk_fma_f32 v[240:241], v[212:213], v[248:249], v[250:251] op_sel:[0,1,0] op_sel_hi:[1,1,0]
	v_pk_fma_f32 v[238:239], v[210:211], v[238:239], v[250:251] op_sel:[0,0,1] op_sel_hi:[1,1,1]
	v_pk_fma_f32 v[240:241], v[212:213], v[240:241], v[250:251] op_sel:[0,0,1] op_sel_hi:[1,1,1]
	v_pk_fma_f32 v[238:239], v[210:211], v[238:239], v[252:253] op_sel:[0,0,0] op_sel_hi:[1,1,0]
	v_pk_fma_f32 v[240:241], v[212:213], v[240:241], v[252:253] op_sel:[0,0,0] op_sel_hi:[1,1,0]
	v_pk_fma_f32 v[238:239], v[210:211], v[238:239], v[248:249] op_sel:[0,0,0] op_sel_hi:[1,1,0]
	v_pk_fma_f32 v[240:241], v[212:213], v[240:241], v[248:249] op_sel:[0,0,0] op_sel_hi:[1,1,0]
	v_pk_mul_f32 v[238:239], v[210:211], v[238:239] op_sel:[0,0] op_sel_hi:[1,1] neg_lo:[1,0] neg_hi:[1,0]
	v_pk_mul_f32 v[240:241], v[212:213], v[240:241] op_sel:[0,0] op_sel_hi:[1,1] neg_lo:[1,0] neg_hi:[1,0]
	v_pk_fma_f32 v[242:243], v[214:215], v[214:215], v[248:249] op_sel:[0,0,0] op_sel_hi:[1,1,0] neg_lo:[1,0,0] neg_hi:[1,0,0]
	v_pk_fma_f32 v[244:245], v[216:217], v[216:217], v[248:249] op_sel:[0,0,0] op_sel_hi:[1,1,0] neg_lo:[1,0,0] neg_hi:[1,0,0]
	v_cmp_lt_f32_e64 s[24:25], v253, v210
	v_cmp_lt_f32_e64 s[26:27], v253, v211
	v_cmp_lt_f32_e64 s[30:31], v253, v212
	v_cmp_lt_f32_e64 s[34:35], v253, v213
	v_cndmask_b32_e64 v238, v242, v238, s[24:25]
	v_cndmask_b32_e64 v239, v243, v239, s[26:27]
	v_cndmask_b32_e64 v240, v244, v240, s[30:31]
	v_cndmask_b32_e64 v241, v245, v241, s[34:35]
	v_sqrt_f32_e32 v238, v238
	v_sqrt_f32_e32 v239, v239
	v_sqrt_f32_e32 v240, v240
	v_sqrt_f32_e32 v241, v241
	v_pk_mul_f32 v[206:207], v[238:239], v[206:207] op_sel:[0,0] op_sel_hi:[1,1]
	v_pk_mul_f32 v[208:209], v[240:241], v[208:209] op_sel:[0,0] op_sel_hi:[1,1]
	v_pk_fma_f32 v[124:125], v[214:215], v[128:129], v[206:207] op_sel:[0,0,0] op_sel_hi:[1,1,1]
	v_pk_fma_f32 v[126:127], v[216:217], v[130:131], v[208:209] op_sel:[0,0,0] op_sel_hi:[1,1,1]
	v_pk_mul_f32 v[140:141], v[144:145], v[214:215] op_sel:[0,0] op_sel_hi:[1,1]
	v_pk_mul_f32 v[142:143], v[146:147], v[216:217] op_sel:[0,0] op_sel_hi:[1,1]
	v_pk_add_f32 v[202:203], v[108:109], v[72:73] op_sel:[0,0] op_sel_hi:[1,1]
	v_pk_add_f32 v[204:205], v[110:111], v[74:75] op_sel:[0,0] op_sel_hi:[1,1]
	v_pk_add_f32 v[206:207], v[80:81], v[104:105] op_sel:[0,0] op_sel_hi:[1,1]
	v_pk_add_f32 v[208:209], v[82:83], v[106:107] op_sel:[0,0] op_sel_hi:[1,1]
	v_pk_mul_f32 v[202:203], v[202:203], v[246:247] op_sel:[0,0] op_sel_hi:[1,0]
	v_pk_mul_f32 v[204:205], v[204:205], v[246:247] op_sel:[0,0] op_sel_hi:[1,0]
	v_pk_mul_f32 v[206:207], v[206:207], v[246:247] op_sel:[0,0] op_sel_hi:[1,0]
	v_pk_mul_f32 v[208:209], v[208:209], v[246:247] op_sel:[0,0] op_sel_hi:[1,0]
	v_exp_f32_e32 v202, v202
	v_exp_f32_e32 v203, v203
	v_exp_f32_e32 v204, v204
	v_exp_f32_e32 v205, v205
	v_exp_f32_e32 v206, v206
	v_exp_f32_e32 v207, v207
	v_exp_f32_e32 v208, v208
	v_exp_f32_e32 v209, v209
	v_pk_add_f32 v[202:203], v[202:203], v[248:249] op_sel:[0,0] op_sel_hi:[1,0]
	v_pk_add_f32 v[204:205], v[204:205], v[248:249] op_sel:[0,0] op_sel_hi:[1,0]
	v_pk_add_f32 v[206:207], v[206:207], v[248:249] op_sel:[0,0] op_sel_hi:[1,0]
	v_pk_add_f32 v[208:209], v[208:209], v[248:249] op_sel:[0,0] op_sel_hi:[1,0]
	v_rcp_f32_e32 v202, v202
	v_rcp_f32_e32 v203, v203
	v_rcp_f32_e32 v204, v204
	v_rcp_f32_e32 v205, v205
	v_rcp_f32_e32 v206, v206
	v_rcp_f32_e32 v207, v207
	v_rcp_f32_e32 v208, v208
	v_rcp_f32_e32 v209, v209
	s_waitcnt vmcnt(15)
; __device__ __forceinline__ float fast_exp(float x) { return __builtin_amdgcn_exp2f(x * 1.4426950408889634f); }
; __device__ __forceinline__ float fast_sigmoid(float x) { return __builtin_amdgcn_rcpf(1.0f + fast_exp(-x)); }
;     __device__ __forceinline__ void operator()(Acc& acc, const Unit& u, int wr, int wc, int fr_, int fq_, LAS unsigned char* le, int wid, int lane, int&) const {
;     ...
;                 for (int n = 0; n < 2; ++n) {
;                     const f32x4 ba = *(const f32x4*)(b_a + ch0 + n * 16), bi = *(const f32x4*)(b_i + ch0 + n * 16), sl = *(const f32x4*)(spl + ch0 + n * 16);
;                     const u32x2 xw = xpre[ai][m][n]; const float xv[4] = {bflo(xw.x), bfhi(xw.x), bflo(xw.y), bfhi(xw.y)};
;                     const f32x4 ra = acc[ai][0][m][n] + ba, ri = acc[ai][1][m][n] + bi;
; #pragma unroll
;                     for (int j = 0; j < 4; ++j) { const float r = fast_sigmoid(ra[j]), ig = fast_sigmoid(ri[j]);
;                         const float la = -8.0f * r * sl[j];
;                         const float a = fast_exp(la); const float x2 = 2.0f * la;
;                         const float ser = -x2 * (1.0f + x2 * (0.5f + x2 * (1.0f / 6.0f + x2 * (1.0f / 24.0f + x2 * (1.0f / 120.0f)))));
;                         const float om = (x2 > -0.3f) ? ser : (1.0f - a * a);
;                         const float uu = __builtin_amdgcn_sqrtf(om) * (ig * xv[j]);
;                         if (m == 0) { acc[ai][0][m][n][j] = a; acc[ai][1][m][n][j] = uu; }
;                         else { acc[ai][1][m][n][j] = a * acc[ai][1][m - 1][n][j] + uu; acc[ai][0][m][n][j] = acc[ai][0][m - 1][n][j] * a; } } } }
;     ...
;         u32x2 gpre[2][4][2];
; #pragma unroll
;         for (int m = 0; m < 4; ++m)
; #pragma unroll
;             for (int n = 0; n < 2; ++n) gpre[0][m][n] = *(const u32x2*)(gg + roff + (size_t)m * DM + n * 16);
	v_lshlrev_b32_e32 v242, 16, v176
	v_and_b32_e32 v243, s22, v176
	v_lshlrev_b32_e32 v244, 16, v177
	v_and_b32_e32 v245, s22, v177
	global_load_dwordx2 v[176:177], v231, s[46:47] offset:32
	v_pk_mul_f32 v[210:211], v[202:203], v[198:199] op_sel:[0,0] op_sel_hi:[1,1]
	v_pk_mul_f32 v[212:213], v[204:205], v[200:201] op_sel:[0,0] op_sel_hi:[1,1]
	v_pk_mul_f32 v[206:207], v[206:207], v[242:243] op_sel:[0,0] op_sel_hi:[1,1]
	v_pk_mul_f32 v[208:209], v[208:209], v[244:245] op_sel:[0,0] op_sel_hi:[1,1]
	v_pk_mul_f32 v[214:215], v[210:211], v[246:247] op_sel:[0,1] op_sel_hi:[1,1]
	v_pk_mul_f32 v[216:217], v[212:213], v[246:247] op_sel:[0,1] op_sel_hi:[1,1]
	v_pk_add_f32 v[210:211], v[210:211], v[210:211] op_sel:[0,0] op_sel_hi:[1,1]
	v_pk_add_f32 v[212:213], v[212:213], v[212:213] op_sel:[0,0] op_sel_hi:[1,1]
	v_exp_f32_e32 v214, v214
	v_exp_f32_e32 v215, v215
	v_exp_f32_e32 v216, v216
	v_exp_f32_e32 v217, v217
	v_pk_fma_f32 v[238:239], v[210:211], v[248:249], v[250:251] op_sel:[0,1,0] op_sel_hi:[1,1,0]
	v_pk_fma_f32 v[240:241], v[212:213], v[248:249], v[250:251] op_sel:[0,1,0] op_sel_hi:[1,1,0]
	v_pk_fma_f32 v[238:239], v[210:211], v[238:239], v[250:251] op_sel:[0,0,1] op_sel_hi:[1,1,1]
	v_pk_fma_f32 v[240:241], v[212:213], v[240:241], v[250:251] op_sel:[0,0,1] op_sel_hi:[1,1,1]
	v_pk_fma_f32 v[238:239], v[210:211], v[238:239], v[252:253] op_sel:[0,0,0] op_sel_hi:[1,1,0]
	v_pk_fma_f32 v[240:241], v[212:213], v[240:241], v[252:253] op_sel:[0,0,0] op_sel_hi:[1,1,0]
	v_pk_fma_f32 v[238:239], v[210:211], v[238:239], v[248:249] op_sel:[0,0,0] op_sel_hi:[1,1,0]
	v_pk_fma_f32 v[240:241], v[212:213], v[240:241], v[248:249] op_sel:[0,0,0] op_sel_hi:[1,1,0]
	v_pk_mul_f32 v[238:239], v[210:211], v[238:239] op_sel:[0,0] op_sel_hi:[1,1] neg_lo:[1,0] neg_hi:[1,0]
	v_pk_mul_f32 v[240:241], v[212:213], v[240:241] op_sel:[0,0] op_sel_hi:[1,1] neg_lo:[1,0] neg_hi:[1,0]
	v_pk_fma_f32 v[242:243], v[214:215], v[214:215], v[248:249] op_sel:[0,0,0] op_sel_hi:[1,1,0] neg_lo:[1,0,0] neg_hi:[1,0,0]
	v_pk_fma_f32 v[244:245], v[216:217], v[216:217], v[248:249] op_sel:[0,0,0] op_sel_hi:[1,1,0] neg_lo:[1,0,0] neg_hi:[1,0,0]
	v_cmp_lt_f32_e64 s[24:25], v253, v210
	v_cmp_lt_f32_e64 s[26:27], v253, v211
	v_cmp_lt_f32_e64 s[30:31], v253, v212
	v_cmp_lt_f32_e64 s[34:35], v253, v213
	v_cndmask_b32_e64 v238, v242, v238, s[24:25]
	v_cndmask_b32_e64 v239, v243, v239, s[26:27]
	v_cndmask_b32_e64 v240, v244, v240, s[30:31]
	v_cndmask_b32_e64 v241, v245, v241, s[34:35]
	v_sqrt_f32_e32 v238, v238
	v_sqrt_f32_e32 v239, v239
	v_sqrt_f32_e32 v240, v240
	v_sqrt_f32_e32 v241, v241
	v_pk_mul_f32 v[206:207], v[238:239], v[206:207] op_sel:[0,0] op_sel_hi:[1,1]
	v_pk_mul_f32 v[208:209], v[240:241], v[208:209] op_sel:[0,0] op_sel_hi:[1,1]
	v_pk_fma_f32 v[80:81], v[214:215], v[84:85], v[206:207] op_sel:[0,0,0] op_sel_hi:[1,1,1]
	v_pk_fma_f32 v[82:83], v[216:217], v[86:87], v[208:209] op_sel:[0,0,0] op_sel_hi:[1,1,1]
	v_pk_mul_f32 v[108:109], v[112:113], v[214:215] op_sel:[0,0] op_sel_hi:[1,1]
	v_pk_mul_f32 v[110:111], v[114:115], v[216:217] op_sel:[0,0] op_sel_hi:[1,1]
	v_pk_add_f32 v[202:203], v[136:137], v[68:69] op_sel:[0,0] op_sel_hi:[1,1]
	v_pk_add_f32 v[204:205], v[138:139], v[70:71] op_sel:[0,0] op_sel_hi:[1,1]
	v_pk_add_f32 v[206:207], v[120:121], v[100:101] op_sel:[0,0] op_sel_hi:[1,1]
	v_pk_add_f32 v[208:209], v[122:123], v[102:103] op_sel:[0,0] op_sel_hi:[1,1]
	v_pk_mul_f32 v[202:203], v[202:203], v[246:247] op_sel:[0,0] op_sel_hi:[1,0]
	v_pk_mul_f32 v[204:205], v[204:205], v[246:247] op_sel:[0,0] op_sel_hi:[1,0]
	v_pk_mul_f32 v[206:207], v[206:207], v[246:247] op_sel:[0,0] op_sel_hi:[1,0]
	v_pk_mul_f32 v[208:209], v[208:209], v[246:247] op_sel:[0,0] op_sel_hi:[1,0]
	v_exp_f32_e32 v202, v202
	v_exp_f32_e32 v203, v203
	v_exp_f32_e32 v204, v204
	v_exp_f32_e32 v205, v205
	v_exp_f32_e32 v206, v206
	v_exp_f32_e32 v207, v207
	v_exp_f32_e32 v208, v208
	v_exp_f32_e32 v209, v209
	v_pk_add_f32 v[202:203], v[202:203], v[248:249] op_sel:[0,0] op_sel_hi:[1,0]
	v_pk_add_f32 v[204:205], v[204:205], v[248:249] op_sel:[0,0] op_sel_hi:[1,0]
	v_pk_add_f32 v[206:207], v[206:207], v[248:249] op_sel:[0,0] op_sel_hi:[1,0]
	v_pk_add_f32 v[208:209], v[208:209], v[248:249] op_sel:[0,0] op_sel_hi:[1,0]
	v_rcp_f32_e32 v202, v202
	v_rcp_f32_e32 v203, v203
	v_rcp_f32_e32 v204, v204
	v_rcp_f32_e32 v205, v205
	v_rcp_f32_e32 v206, v206
	v_rcp_f32_e32 v207, v207
	v_rcp_f32_e32 v208, v208
	v_rcp_f32_e32 v209, v209
	s_waitcnt vmcnt(15)
; __device__ __forceinline__ float fast_exp(float x) { return __builtin_amdgcn_exp2f(x * 1.4426950408889634f); }
; __device__ __forceinline__ float fast_sigmoid(float x) { return __builtin_amdgcn_rcpf(1.0f + fast_exp(-x)); }
;     __device__ __forceinline__ void operator()(Acc& acc, const Unit& u, int wr, int wc, int fr_, int fq_, LAS unsigned char* le, int wid, int lane, int&) const {
;     ...
;                 for (int n = 0; n < 2; ++n) {
;                     const f32x4 ba = *(const f32x4*)(b_a + ch0 + n * 16), bi = *(const f32x4*)(b_i + ch0 + n * 16), sl = *(const f32x4*)(spl + ch0 + n * 16);
;                     const u32x2 xw = xpre[ai][m][n]; const float xv[4] = {bflo(xw.x), bfhi(xw.x), bflo(xw.y), bfhi(xw.y)};
;                     const f32x4 ra = acc[ai][0][m][n] + ba, ri = acc[ai][1][m][n] + bi;
; #pragma unroll
;                     for (int j = 0; j < 4; ++j) { const float r = fast_sigmoid(ra[j]), ig = fast_sigmoid(ri[j]);
;                         const float la = -8.0f * r * sl[j];
;                         const float a = fast_exp(la); const float x2 = 2.0f * la;
;                         const float ser = -x2 * (1.0f + x2 * (0.5f + x2 * (1.0f / 6.0f + x2 * (1.0f / 24.0f + x2 * (1.0f / 120.0f)))));
;                         const float om = (x2 > -0.3f) ? ser : (1.0f - a * a);
;                         const float uu = __builtin_amdgcn_sqrtf(om) * (ig * xv[j]);
;                         if (m == 0) { acc[ai][0][m][n][j] = a; acc[ai][1][m][n][j] = uu; }
;                         else { acc[ai][1][m][n][j] = a * acc[ai][1][m - 1][n][j] + uu; acc[ai][0][m][n][j] = acc[ai][0][m - 1][n][j] * a; } } } }
;     ...
;         u32x2 gpre[2][4][2];
; #pragma unroll
;         for (int m = 0; m < 4; ++m)
; #pragma unroll
;             for (int n = 0; n < 2; ++n) gpre[0][m][n] = *(const u32x2*)(gg + roff + (size_t)m * DM + n * 16);
	v_lshlrev_b32_e32 v242, 16, v178
	v_and_b32_e32 v243, s22, v178
	v_lshlrev_b32_e32 v244, 16, v179
	v_and_b32_e32 v245, s22, v179
	global_load_dwordx2 v[178:179], v232, s[46:47] offset:0
	v_pk_mul_f32 v[210:211], v[202:203], v[88:89] op_sel:[0,0] op_sel_hi:[1,1]
	v_pk_mul_f32 v[212:213], v[204:205], v[90:91] op_sel:[0,0] op_sel_hi:[1,1]
	v_pk_mul_f32 v[206:207], v[206:207], v[242:243] op_sel:[0,0] op_sel_hi:[1,1]
	v_pk_mul_f32 v[208:209], v[208:209], v[244:245] op_sel:[0,0] op_sel_hi:[1,1]
	v_pk_mul_f32 v[214:215], v[210:211], v[246:247] op_sel:[0,1] op_sel_hi:[1,1]
	v_pk_mul_f32 v[216:217], v[212:213], v[246:247] op_sel:[0,1] op_sel_hi:[1,1]
	v_pk_add_f32 v[210:211], v[210:211], v[210:211] op_sel:[0,0] op_sel_hi:[1,1]
	v_pk_add_f32 v[212:213], v[212:213], v[212:213] op_sel:[0,0] op_sel_hi:[1,1]
	v_exp_f32_e32 v214, v214
	v_exp_f32_e32 v215, v215
	v_exp_f32_e32 v216, v216
	v_exp_f32_e32 v217, v217
	v_pk_fma_f32 v[238:239], v[210:211], v[248:249], v[250:251] op_sel:[0,1,0] op_sel_hi:[1,1,0]
	v_pk_fma_f32 v[240:241], v[212:213], v[248:249], v[250:251] op_sel:[0,1,0] op_sel_hi:[1,1,0]
	v_pk_fma_f32 v[238:239], v[210:211], v[238:239], v[250:251] op_sel:[0,0,1] op_sel_hi:[1,1,1]
	v_pk_fma_f32 v[240:241], v[212:213], v[240:241], v[250:251] op_sel:[0,0,1] op_sel_hi:[1,1,1]
	v_pk_fma_f32 v[238:239], v[210:211], v[238:239], v[252:253] op_sel:[0,0,0] op_sel_hi:[1,1,0]
	v_pk_fma_f32 v[240:241], v[212:213], v[240:241], v[252:253] op_sel:[0,0,0] op_sel_hi:[1,1,0]
	v_pk_fma_f32 v[238:239], v[210:211], v[238:239], v[248:249] op_sel:[0,0,0] op_sel_hi:[1,1,0]
	v_pk_fma_f32 v[240:241], v[212:213], v[240:241], v[248:249] op_sel:[0,0,0] op_sel_hi:[1,1,0]
	v_pk_mul_f32 v[238:239], v[210:211], v[238:239] op_sel:[0,0] op_sel_hi:[1,1] neg_lo:[1,0] neg_hi:[1,0]
	v_pk_mul_f32 v[240:241], v[212:213], v[240:241] op_sel:[0,0] op_sel_hi:[1,1] neg_lo:[1,0] neg_hi:[1,0]
	v_pk_fma_f32 v[242:243], v[214:215], v[214:215], v[248:249] op_sel:[0,0,0] op_sel_hi:[1,1,0] neg_lo:[1,0,0] neg_hi:[1,0,0]
	v_pk_fma_f32 v[244:245], v[216:217], v[216:217], v[248:249] op_sel:[0,0,0] op_sel_hi:[1,1,0] neg_lo:[1,0,0] neg_hi:[1,0,0]
	v_cmp_lt_f32_e64 s[24:25], v253, v210
	v_cmp_lt_f32_e64 s[26:27], v253, v211
	v_cmp_lt_f32_e64 s[30:31], v253, v212
	v_cmp_lt_f32_e64 s[34:35], v253, v213
	v_cndmask_b32_e64 v238, v242, v238, s[24:25]
	v_cndmask_b32_e64 v239, v243, v239, s[26:27]
	v_cndmask_b32_e64 v240, v244, v240, s[30:31]
	v_cndmask_b32_e64 v241, v245, v241, s[34:35]
	v_sqrt_f32_e32 v238, v238
	v_sqrt_f32_e32 v239, v239
	v_sqrt_f32_e32 v240, v240
	v_sqrt_f32_e32 v241, v241
	v_pk_mul_f32 v[206:207], v[238:239], v[206:207] op_sel:[0,0] op_sel_hi:[1,1]
	v_pk_mul_f32 v[208:209], v[240:241], v[208:209] op_sel:[0,0] op_sel_hi:[1,1]
	v_pk_fma_f32 v[120:121], v[214:215], v[124:125], v[206:207] op_sel:[0,0,0] op_sel_hi:[1,1,1]
	v_pk_fma_f32 v[122:123], v[216:217], v[126:127], v[208:209] op_sel:[0,0,0] op_sel_hi:[1,1,1]
	v_pk_mul_f32 v[136:137], v[140:141], v[214:215] op_sel:[0,0] op_sel_hi:[1,1]
	v_pk_mul_f32 v[138:139], v[142:143], v[216:217] op_sel:[0,0] op_sel_hi:[1,1]
	v_pk_add_f32 v[202:203], v[96:97], v[72:73] op_sel:[0,0] op_sel_hi:[1,1]
	v_pk_add_f32 v[204:205], v[98:99], v[74:75] op_sel:[0,0] op_sel_hi:[1,1]
	v_pk_add_f32 v[206:207], v[76:77], v[104:105] op_sel:[0,0] op_sel_hi:[1,1]
	v_pk_add_f32 v[208:209], v[78:79], v[106:107] op_sel:[0,0] op_sel_hi:[1,1]
	v_pk_mul_f32 v[202:203], v[202:203], v[246:247] op_sel:[0,0] op_sel_hi:[1,0]
	v_pk_mul_f32 v[204:205], v[204:205], v[246:247] op_sel:[0,0] op_sel_hi:[1,0]
	v_pk_mul_f32 v[206:207], v[206:207], v[246:247] op_sel:[0,0] op_sel_hi:[1,0]
	v_pk_mul_f32 v[208:209], v[208:209], v[246:247] op_sel:[0,0] op_sel_hi:[1,0]
	v_exp_f32_e32 v202, v202
	v_exp_f32_e32 v203, v203
	v_exp_f32_e32 v204, v204
	v_exp_f32_e32 v205, v205
	v_exp_f32_e32 v206, v206
	v_exp_f32_e32 v207, v207
	v_exp_f32_e32 v208, v208
	v_exp_f32_e32 v209, v209
	v_pk_add_f32 v[202:203], v[202:203], v[248:249] op_sel:[0,0] op_sel_hi:[1,0]
	v_pk_add_f32 v[204:205], v[204:205], v[248:249] op_sel:[0,0] op_sel_hi:[1,0]
	v_pk_add_f32 v[206:207], v[206:207], v[248:249] op_sel:[0,0] op_sel_hi:[1,0]
	v_pk_add_f32 v[208:209], v[208:209], v[248:249] op_sel:[0,0] op_sel_hi:[1,0]
	v_rcp_f32_e32 v202, v202
	v_rcp_f32_e32 v203, v203
	v_rcp_f32_e32 v204, v204
	v_rcp_f32_e32 v205, v205
	v_rcp_f32_e32 v206, v206
	v_rcp_f32_e32 v207, v207
	v_rcp_f32_e32 v208, v208
	v_rcp_f32_e32 v209, v209
	s_waitcnt vmcnt(15)
; __device__ __forceinline__ float fast_exp(float x) { return __builtin_amdgcn_exp2f(x * 1.4426950408889634f); }
; __device__ __forceinline__ float fast_sigmoid(float x) { return __builtin_amdgcn_rcpf(1.0f + fast_exp(-x)); }
;     __device__ __forceinline__ void operator()(Acc& acc, const Unit& u, int wr, int wc, int fr_, int fq_, LAS unsigned char* le, int wid, int lane, int&) const {
;     ...
;                 for (int n = 0; n < 2; ++n) {
;                     const f32x4 ba = *(const f32x4*)(b_a + ch0 + n * 16), bi = *(const f32x4*)(b_i + ch0 + n * 16), sl = *(const f32x4*)(spl + ch0 + n * 16);
;                     const u32x2 xw = xpre[ai][m][n]; const float xv[4] = {bflo(xw.x), bfhi(xw.x), bflo(xw.y), bfhi(xw.y)};
;                     const f32x4 ra = acc[ai][0][m][n] + ba, ri = acc[ai][1][m][n] + bi;
; #pragma unroll
;                     for (int j = 0; j < 4; ++j) { const float r = fast_sigmoid(ra[j]), ig = fast_sigmoid(ri[j]);
;                         const float la = -8.0f * r * sl[j];
;                         const float a = fast_exp(la); const float x2 = 2.0f * la;
;                         const float ser = -x2 * (1.0f + x2 * (0.5f + x2 * (1.0f / 6.0f + x2 * (1.0f / 24.0f + x2 * (1.0f / 120.0f)))));
;                         const float om = (x2 > -0.3f) ? ser : (1.0f - a * a);
;                         const float uu = __builtin_amdgcn_sqrtf(om) * (ig * xv[j]);
;                         if (m == 0) { acc[ai][0][m][n][j] = a; acc[ai][1][m][n][j] = uu; }
;                         else { acc[ai][1][m][n][j] = a * acc[ai][1][m - 1][n][j] + uu; acc[ai][0][m][n][j] = acc[ai][0][m - 1][n][j] * a; } } } }
;     ...
;         u32x2 gpre[2][4][2];
; #pragma unroll
;         for (int m = 0; m < 4; ++m)
; #pragma unroll
;             for (int n = 0; n < 2; ++n) gpre[0][m][n] = *(const u32x2*)(gg + roff + (size_t)m * DM + n * 16);
	v_lshlrev_b32_e32 v242, 16, v180
	v_and_b32_e32 v243, s22, v180
	v_lshlrev_b32_e32 v244, 16, v181
	v_and_b32_e32 v245, s22, v181
	global_load_dwordx2 v[180:181], v232, s[46:47] offset:32
	v_pk_mul_f32 v[210:211], v[202:203], v[198:199] op_sel:[0,0] op_sel_hi:[1,1]
	v_pk_mul_f32 v[212:213], v[204:205], v[200:201] op_sel:[0,0] op_sel_hi:[1,1]
	v_pk_mul_f32 v[206:207], v[206:207], v[242:243] op_sel:[0,0] op_sel_hi:[1,1]
	v_pk_mul_f32 v[208:209], v[208:209], v[244:245] op_sel:[0,0] op_sel_hi:[1,1]
	v_pk_mul_f32 v[214:215], v[210:211], v[246:247] op_sel:[0,1] op_sel_hi:[1,1]
	v_pk_mul_f32 v[216:217], v[212:213], v[246:247] op_sel:[0,1] op_sel_hi:[1,1]
	v_pk_add_f32 v[210:211], v[210:211], v[210:211] op_sel:[0,0] op_sel_hi:[1,1]
	v_pk_add_f32 v[212:213], v[212:213], v[212:213] op_sel:[0,0] op_sel_hi:[1,1]
	v_exp_f32_e32 v214, v214
	v_exp_f32_e32 v215, v215
	v_exp_f32_e32 v216, v216
	v_exp_f32_e32 v217, v217
	v_pk_fma_f32 v[238:239], v[210:211], v[248:249], v[250:251] op_sel:[0,1,0] op_sel_hi:[1,1,0]
	v_pk_fma_f32 v[240:241], v[212:213], v[248:249], v[250:251] op_sel:[0,1,0] op_sel_hi:[1,1,0]
	v_pk_fma_f32 v[238:239], v[210:211], v[238:239], v[250:251] op_sel:[0,0,1] op_sel_hi:[1,1,1]
	v_pk_fma_f32 v[240:241], v[212:213], v[240:241], v[250:251] op_sel:[0,0,1] op_sel_hi:[1,1,1]
	v_pk_fma_f32 v[238:239], v[210:211], v[238:239], v[252:253] op_sel:[0,0,0] op_sel_hi:[1,1,0]
	v_pk_fma_f32 v[240:241], v[212:213], v[240:241], v[252:253] op_sel:[0,0,0] op_sel_hi:[1,1,0]
	v_pk_fma_f32 v[238:239], v[210:211], v[238:239], v[248:249] op_sel:[0,0,0] op_sel_hi:[1,1,0]
	v_pk_fma_f32 v[240:241], v[212:213], v[240:241], v[248:249] op_sel:[0,0,0] op_sel_hi:[1,1,0]
	v_pk_mul_f32 v[238:239], v[210:211], v[238:239] op_sel:[0,0] op_sel_hi:[1,1] neg_lo:[1,0] neg_hi:[1,0]
	v_pk_mul_f32 v[240:241], v[212:213], v[240:241] op_sel:[0,0] op_sel_hi:[1,1] neg_lo:[1,0] neg_hi:[1,0]
	v_pk_fma_f32 v[242:243], v[214:215], v[214:215], v[248:249] op_sel:[0,0,0] op_sel_hi:[1,1,0] neg_lo:[1,0,0] neg_hi:[1,0,0]
	v_pk_fma_f32 v[244:245], v[216:217], v[216:217], v[248:249] op_sel:[0,0,0] op_sel_hi:[1,1,0] neg_lo:[1,0,0] neg_hi:[1,0,0]
	v_cmp_lt_f32_e64 s[24:25], v253, v210
	v_cmp_lt_f32_e64 s[26:27], v253, v211
	v_cmp_lt_f32_e64 s[30:31], v253, v212
	v_cmp_lt_f32_e64 s[34:35], v253, v213
	v_cndmask_b32_e64 v238, v242, v238, s[24:25]
	v_cndmask_b32_e64 v239, v243, v239, s[26:27]
	v_cndmask_b32_e64 v240, v244, v240, s[30:31]
	v_cndmask_b32_e64 v241, v245, v241, s[34:35]
	v_sqrt_f32_e32 v238, v238
	v_sqrt_f32_e32 v239, v239
	v_sqrt_f32_e32 v240, v240
	v_sqrt_f32_e32 v241, v241
	v_pk_mul_f32 v[206:207], v[238:239], v[206:207] op_sel:[0,0] op_sel_hi:[1,1]
	v_pk_mul_f32 v[208:209], v[240:241], v[208:209] op_sel:[0,0] op_sel_hi:[1,1]
	v_pk_fma_f32 v[76:77], v[214:215], v[80:81], v[206:207] op_sel:[0,0,0] op_sel_hi:[1,1,1]
	v_pk_fma_f32 v[78:79], v[216:217], v[82:83], v[208:209] op_sel:[0,0,0] op_sel_hi:[1,1,1]
	v_pk_mul_f32 v[96:97], v[108:109], v[214:215] op_sel:[0,0] op_sel_hi:[1,1]
	v_pk_mul_f32 v[98:99], v[110:111], v[216:217] op_sel:[0,0] op_sel_hi:[1,1]
	v_pk_add_f32 v[202:203], v[64:65], v[68:69] op_sel:[0,0] op_sel_hi:[1,1]
	v_pk_add_f32 v[204:205], v[66:67], v[70:71] op_sel:[0,0] op_sel_hi:[1,1]
	v_pk_add_f32 v[206:207], v[44:45], v[100:101] op_sel:[0,0] op_sel_hi:[1,1]
	v_pk_add_f32 v[208:209], v[46:47], v[102:103] op_sel:[0,0] op_sel_hi:[1,1]
	v_pk_mul_f32 v[202:203], v[202:203], v[246:247] op_sel:[0,0] op_sel_hi:[1,0]
	v_pk_mul_f32 v[204:205], v[204:205], v[246:247] op_sel:[0,0] op_sel_hi:[1,0]
	v_pk_mul_f32 v[206:207], v[206:207], v[246:247] op_sel:[0,0] op_sel_hi:[1,0]
	v_pk_mul_f32 v[208:209], v[208:209], v[246:247] op_sel:[0,0] op_sel_hi:[1,0]
	v_exp_f32_e32 v202, v202
	v_exp_f32_e32 v203, v203
	v_exp_f32_e32 v204, v204
	v_exp_f32_e32 v205, v205
	v_exp_f32_e32 v206, v206
	v_exp_f32_e32 v207, v207
	v_exp_f32_e32 v208, v208
	v_exp_f32_e32 v209, v209
	v_pk_add_f32 v[202:203], v[202:203], v[248:249] op_sel:[0,0] op_sel_hi:[1,0]
	v_pk_add_f32 v[204:205], v[204:205], v[248:249] op_sel:[0,0] op_sel_hi:[1,0]
	v_pk_add_f32 v[206:207], v[206:207], v[248:249] op_sel:[0,0] op_sel_hi:[1,0]
	v_pk_add_f32 v[208:209], v[208:209], v[248:249] op_sel:[0,0] op_sel_hi:[1,0]
	v_rcp_f32_e32 v202, v202
	v_rcp_f32_e32 v203, v203
	v_rcp_f32_e32 v204, v204
	v_rcp_f32_e32 v205, v205
	v_rcp_f32_e32 v206, v206
	v_rcp_f32_e32 v207, v207
	v_rcp_f32_e32 v208, v208
	v_rcp_f32_e32 v209, v209
	s_waitcnt vmcnt(15)
; __device__ __forceinline__ float fast_exp(float x) { return __builtin_amdgcn_exp2f(x * 1.4426950408889634f); }
; __device__ __forceinline__ float fast_sigmoid(float x) { return __builtin_amdgcn_rcpf(1.0f + fast_exp(-x)); }
;     __device__ __forceinline__ void operator()(Acc& acc, const Unit& u, int wr, int wc, int fr_, int fq_, LAS unsigned char* le, int wid, int lane, int&) const {
;     ...
;                 for (int n = 0; n < 2; ++n) {
;                     const f32x4 ba = *(const f32x4*)(b_a + ch0 + n * 16), bi = *(const f32x4*)(b_i + ch0 + n * 16), sl = *(const f32x4*)(spl + ch0 + n * 16);
;                     const u32x2 xw = xpre[ai][m][n]; const float xv[4] = {bflo(xw.x), bfhi(xw.x), bflo(xw.y), bfhi(xw.y)};
;                     const f32x4 ra = acc[ai][0][m][n] + ba, ri = acc[ai][1][m][n] + bi;
; #pragma unroll
;                     for (int j = 0; j < 4; ++j) { const float r = fast_sigmoid(ra[j]), ig = fast_sigmoid(ri[j]);
;                         const float la = -8.0f * r * sl[j];
;                         const float a = fast_exp(la); const float x2 = 2.0f * la;
;                         const float ser = -x2 * (1.0f + x2 * (0.5f + x2 * (1.0f / 6.0f + x2 * (1.0f / 24.0f + x2 * (1.0f / 120.0f)))));
;                         const float om = (x2 > -0.3f) ? ser : (1.0f - a * a);
;                         const float uu = __builtin_amdgcn_sqrtf(om) * (ig * xv[j]);
;                         if (m == 0) { acc[ai][0][m][n][j] = a; acc[ai][1][m][n][j] = uu; }
;                         else { acc[ai][1][m][n][j] = a * acc[ai][1][m - 1][n][j] + uu; acc[ai][0][m][n][j] = acc[ai][0][m - 1][n][j] * a; } } } }
;     ...
;         u32x2 gpre[2][4][2];
; #pragma unroll
;         for (int m = 0; m < 4; ++m)
; #pragma unroll
;             for (int n = 0; n < 2; ++n) gpre[0][m][n] = *(const u32x2*)(gg + roff + (size_t)m * DM + n * 16);
	v_lshlrev_b32_e32 v242, 16, v182
	v_and_b32_e32 v243, s22, v182
	v_lshlrev_b32_e32 v244, 16, v183
	v_and_b32_e32 v245, s22, v183
	global_load_dwordx2 v[182:183], v233, s[46:47] offset:0
	v_pk_mul_f32 v[210:211], v[202:203], v[88:89] op_sel:[0,0] op_sel_hi:[1,1]
	v_pk_mul_f32 v[212:213], v[204:205], v[90:91] op_sel:[0,0] op_sel_hi:[1,1]
	v_pk_mul_f32 v[206:207], v[206:207], v[242:243] op_sel:[0,0] op_sel_hi:[1,1]
	v_pk_mul_f32 v[208:209], v[208:209], v[244:245] op_sel:[0,0] op_sel_hi:[1,1]
	v_pk_mul_f32 v[214:215], v[210:211], v[246:247] op_sel:[0,1] op_sel_hi:[1,1]
	v_pk_mul_f32 v[216:217], v[212:213], v[246:247] op_sel:[0,1] op_sel_hi:[1,1]
	v_pk_add_f32 v[210:211], v[210:211], v[210:211] op_sel:[0,0] op_sel_hi:[1,1]
	v_pk_add_f32 v[212:213], v[212:213], v[212:213] op_sel:[0,0] op_sel_hi:[1,1]
	v_exp_f32_e32 v64, v214
	v_exp_f32_e32 v65, v215
	v_exp_f32_e32 v66, v216
	v_exp_f32_e32 v67, v217
	v_pk_fma_f32 v[238:239], v[210:211], v[248:249], v[250:251] op_sel:[0,1,0] op_sel_hi:[1,1,0]
	v_pk_fma_f32 v[240:241], v[212:213], v[248:249], v[250:251] op_sel:[0,1,0] op_sel_hi:[1,1,0]
	v_pk_fma_f32 v[238:239], v[210:211], v[238:239], v[250:251] op_sel:[0,0,1] op_sel_hi:[1,1,1]
	v_pk_fma_f32 v[240:241], v[212:213], v[240:241], v[250:251] op_sel:[0,0,1] op_sel_hi:[1,1,1]
	v_pk_fma_f32 v[238:239], v[210:211], v[238:239], v[252:253] op_sel:[0,0,0] op_sel_hi:[1,1,0]
	v_pk_fma_f32 v[240:241], v[212:213], v[240:241], v[252:253] op_sel:[0,0,0] op_sel_hi:[1,1,0]
	v_pk_fma_f32 v[238:239], v[210:211], v[238:239], v[248:249] op_sel:[0,0,0] op_sel_hi:[1,1,0]
	v_pk_fma_f32 v[240:241], v[212:213], v[240:241], v[248:249] op_sel:[0,0,0] op_sel_hi:[1,1,0]
	v_pk_mul_f32 v[238:239], v[210:211], v[238:239] op_sel:[0,0] op_sel_hi:[1,1] neg_lo:[1,0] neg_hi:[1,0]
	v_pk_mul_f32 v[240:241], v[212:213], v[240:241] op_sel:[0,0] op_sel_hi:[1,1] neg_lo:[1,0] neg_hi:[1,0]
	v_pk_fma_f32 v[242:243], v[64:65], v[64:65], v[248:249] op_sel:[0,0,0] op_sel_hi:[1,1,0] neg_lo:[1,0,0] neg_hi:[1,0,0]
	v_pk_fma_f32 v[244:245], v[66:67], v[66:67], v[248:249] op_sel:[0,0,0] op_sel_hi:[1,1,0] neg_lo:[1,0,0] neg_hi:[1,0,0]
	v_cmp_lt_f32_e64 s[24:25], v253, v210
	v_cmp_lt_f32_e64 s[26:27], v253, v211
	v_cmp_lt_f32_e64 s[30:31], v253, v212
	v_cmp_lt_f32_e64 s[34:35], v253, v213
	v_cndmask_b32_e64 v238, v242, v238, s[24:25]
	v_cndmask_b32_e64 v239, v243, v239, s[26:27]
	v_cndmask_b32_e64 v240, v244, v240, s[30:31]
	v_cndmask_b32_e64 v241, v245, v241, s[34:35]
	v_sqrt_f32_e32 v238, v238
	v_sqrt_f32_e32 v239, v239
	v_sqrt_f32_e32 v240, v240
	v_sqrt_f32_e32 v241, v241
	v_pk_mul_f32 v[44:45], v[238:239], v[206:207] op_sel:[0,0] op_sel_hi:[1,1]
	v_pk_mul_f32 v[46:47], v[240:241], v[208:209] op_sel:[0,0] op_sel_hi:[1,1]
	v_pk_add_f32 v[202:203], v[28:29], v[72:73] op_sel:[0,0] op_sel_hi:[1,1]
	v_pk_add_f32 v[204:205], v[30:31], v[74:75] op_sel:[0,0] op_sel_hi:[1,1]
	v_pk_add_f32 v[206:207], v[12:13], v[104:105] op_sel:[0,0] op_sel_hi:[1,1]
	v_pk_add_f32 v[208:209], v[14:15], v[106:107] op_sel:[0,0] op_sel_hi:[1,1]
	v_pk_mul_f32 v[202:203], v[202:203], v[246:247] op_sel:[0,0] op_sel_hi:[1,0]
	v_pk_mul_f32 v[204:205], v[204:205], v[246:247] op_sel:[0,0] op_sel_hi:[1,0]
	v_pk_mul_f32 v[206:207], v[206:207], v[246:247] op_sel:[0,0] op_sel_hi:[1,0]
	v_pk_mul_f32 v[208:209], v[208:209], v[246:247] op_sel:[0,0] op_sel_hi:[1,0]
	v_exp_f32_e32 v202, v202
	v_exp_f32_e32 v203, v203
	v_exp_f32_e32 v204, v204
	v_exp_f32_e32 v205, v205
	v_exp_f32_e32 v206, v206
	v_exp_f32_e32 v207, v207
	v_exp_f32_e32 v208, v208
	v_exp_f32_e32 v209, v209
	v_pk_add_f32 v[202:203], v[202:203], v[248:249] op_sel:[0,0] op_sel_hi:[1,0]
	v_pk_add_f32 v[204:205], v[204:205], v[248:249] op_sel:[0,0] op_sel_hi:[1,0]
	v_pk_add_f32 v[206:207], v[206:207], v[248:249] op_sel:[0,0] op_sel_hi:[1,0]
	v_pk_add_f32 v[208:209], v[208:209], v[248:249] op_sel:[0,0] op_sel_hi:[1,0]
	v_rcp_f32_e32 v202, v202
	v_rcp_f32_e32 v203, v203
	v_rcp_f32_e32 v204, v204
	v_rcp_f32_e32 v205, v205
	v_rcp_f32_e32 v206, v206
	v_rcp_f32_e32 v207, v207
	v_rcp_f32_e32 v208, v208
	v_rcp_f32_e32 v209, v209
	s_waitcnt vmcnt(15)
	v_lshlrev_b32_e32 v242, 16, v184
	v_and_b32_e32 v243, s22, v184
	v_lshlrev_b32_e32 v244, 16, v185
	v_and_b32_e32 v245, s22, v185
	global_load_dwordx2 v[184:185], v233, s[46:47] offset:32
	v_pk_mul_f32 v[210:211], v[202:203], v[198:199] op_sel:[0,0] op_sel_hi:[1,1]
	v_pk_mul_f32 v[212:213], v[204:205], v[200:201] op_sel:[0,0] op_sel_hi:[1,1]
	v_pk_mul_f32 v[206:207], v[206:207], v[242:243] op_sel:[0,0] op_sel_hi:[1,1]
	v_pk_mul_f32 v[208:209], v[208:209], v[244:245] op_sel:[0,0] op_sel_hi:[1,1]
	v_pk_mul_f32 v[214:215], v[210:211], v[246:247] op_sel:[0,1] op_sel_hi:[1,1]
	v_pk_mul_f32 v[216:217], v[212:213], v[246:247] op_sel:[0,1] op_sel_hi:[1,1]
	v_pk_add_f32 v[210:211], v[210:211], v[210:211] op_sel:[0,0] op_sel_hi:[1,1]
	v_pk_add_f32 v[212:213], v[212:213], v[212:213] op_sel:[0,0] op_sel_hi:[1,1]
	v_exp_f32_e32 v28, v214
	v_exp_f32_e32 v29, v215
	v_exp_f32_e32 v30, v216
	v_exp_f32_e32 v31, v217
	v_pk_fma_f32 v[238:239], v[210:211], v[248:249], v[250:251] op_sel:[0,1,0] op_sel_hi:[1,1,0]
	v_pk_fma_f32 v[240:241], v[212:213], v[248:249], v[250:251] op_sel:[0,1,0] op_sel_hi:[1,1,0]
	v_pk_fma_f32 v[238:239], v[210:211], v[238:239], v[250:251] op_sel:[0,0,1] op_sel_hi:[1,1,1]
	v_pk_fma_f32 v[240:241], v[212:213], v[240:241], v[250:251] op_sel:[0,0,1] op_sel_hi:[1,1,1]
	v_pk_fma_f32 v[238:239], v[210:211], v[238:239], v[252:253] op_sel:[0,0,0] op_sel_hi:[1,1,0]
	v_pk_fma_f32 v[240:241], v[212:213], v[240:241], v[252:253] op_sel:[0,0,0] op_sel_hi:[1,1,0]
	v_pk_fma_f32 v[238:239], v[210:211], v[238:239], v[248:249] op_sel:[0,0,0] op_sel_hi:[1,1,0]
; __device__ __forceinline__ float fast_exp(float x) { return __builtin_amdgcn_exp2f(x * 1.4426950408889634f); }
; __device__ __forceinline__ float fast_sigmoid(float x) { return __builtin_amdgcn_rcpf(1.0f + fast_exp(-x)); }
;     __device__ __forceinline__ void operator()(Acc& acc, const Unit& u, int wr, int wc, int fr_, int fq_, LAS unsigned char* le, int wid, int lane, int&) const {
;     ...
;                 for (int n = 0; n < 2; ++n) {
;                     const f32x4 ba = *(const f32x4*)(b_a + ch0 + n * 16), bi = *(const f32x4*)(b_i + ch0 + n * 16), sl = *(const f32x4*)(spl + ch0 + n * 16);
;                     const u32x2 xw = xpre[ai][m][n]; const float xv[4] = {bflo(xw.x), bfhi(xw.x), bflo(xw.y), bfhi(xw.y)};
;                     const f32x4 ra = acc[ai][0][m][n] + ba, ri = acc[ai][1][m][n] + bi;
; #pragma unroll
;                     for (int j = 0; j < 4; ++j) { const float r = fast_sigmoid(ra[j]), ig = fast_sigmoid(ri[j]);
;                         const float la = -8.0f * r * sl[j];
;                         const float a = fast_exp(la); const float x2 = 2.0f * la;
;                         const float ser = -x2 * (1.0f + x2 * (0.5f + x2 * (1.0f / 6.0f + x2 * (1.0f / 24.0f + x2 * (1.0f / 120.0f)))));
;                         const float om = (x2 > -0.3f) ? ser : (1.0f - a * a);
;                         const float uu = __builtin_amdgcn_sqrtf(om) * (ig * xv[j]);
;                         if (m == 0) { acc[ai][0][m][n][j] = a; acc[ai][1][m][n][j] = uu; }
;                         else { acc[ai][1][m][n][j] = a * acc[ai][1][m - 1][n][j] + uu; acc[ai][0][m][n][j] = acc[ai][0][m - 1][n][j] * a; } } } }
;     ...
;         u32x2 gpre[2][4][2];
; #pragma unroll
;         for (int m = 0; m < 4; ++m)
; #pragma unroll
;             for (int n = 0; n < 2; ++n) gpre[0][m][n] = *(const u32x2*)(gg + roff + (size_t)m * DM + n * 16);
	v_pk_fma_f32 v[240:241], v[212:213], v[240:241], v[248:249] op_sel:[0,0,0] op_sel_hi:[1,1,0]
	v_pk_mul_f32 v[238:239], v[210:211], v[238:239] op_sel:[0,0] op_sel_hi:[1,1] neg_lo:[1,0] neg_hi:[1,0]
	v_pk_mul_f32 v[240:241], v[212:213], v[240:241] op_sel:[0,0] op_sel_hi:[1,1] neg_lo:[1,0] neg_hi:[1,0]
	v_pk_fma_f32 v[242:243], v[28:29], v[28:29], v[248:249] op_sel:[0,0,0] op_sel_hi:[1,1,0] neg_lo:[1,0,0] neg_hi:[1,0,0]
	v_pk_fma_f32 v[244:245], v[30:31], v[30:31], v[248:249] op_sel:[0,0,0] op_sel_hi:[1,1,0] neg_lo:[1,0,0] neg_hi:[1,0,0]
	v_cmp_lt_f32_e64 s[24:25], v253, v210
	v_cmp_lt_f32_e64 s[26:27], v253, v211
	v_cmp_lt_f32_e64 s[30:31], v253, v212
	v_cmp_lt_f32_e64 s[34:35], v253, v213
	v_cndmask_b32_e64 v238, v242, v238, s[24:25]
	v_cndmask_b32_e64 v239, v243, v239, s[26:27]
	v_cndmask_b32_e64 v240, v244, v240, s[30:31]
	v_cndmask_b32_e64 v241, v245, v241, s[34:35]
	v_sqrt_f32_e32 v238, v238
	v_sqrt_f32_e32 v239, v239
	v_sqrt_f32_e32 v240, v240
	v_sqrt_f32_e32 v241, v241
	v_pk_mul_f32 v[12:13], v[238:239], v[206:207] op_sel:[0,0] op_sel_hi:[1,1]
	v_pk_mul_f32 v[14:15], v[240:241], v[208:209] op_sel:[0,0] op_sel_hi:[1,1]
	v_pk_add_f32 v[202:203], v[60:61], v[68:69] op_sel:[0,0] op_sel_hi:[1,1]
	v_pk_add_f32 v[204:205], v[62:63], v[70:71] op_sel:[0,0] op_sel_hi:[1,1]
	v_pk_add_f32 v[206:207], v[40:41], v[100:101] op_sel:[0,0] op_sel_hi:[1,1]
	v_pk_add_f32 v[208:209], v[42:43], v[102:103] op_sel:[0,0] op_sel_hi:[1,1]
	v_pk_mul_f32 v[202:203], v[202:203], v[246:247] op_sel:[0,0] op_sel_hi:[1,0]
	v_pk_mul_f32 v[204:205], v[204:205], v[246:247] op_sel:[0,0] op_sel_hi:[1,0]
	v_pk_mul_f32 v[206:207], v[206:207], v[246:247] op_sel:[0,0] op_sel_hi:[1,0]
	v_pk_mul_f32 v[208:209], v[208:209], v[246:247] op_sel:[0,0] op_sel_hi:[1,0]
	v_exp_f32_e32 v202, v202
	v_exp_f32_e32 v203, v203
	v_exp_f32_e32 v204, v204
	v_exp_f32_e32 v205, v205
	v_exp_f32_e32 v206, v206
	v_exp_f32_e32 v207, v207
	v_exp_f32_e32 v208, v208
	v_exp_f32_e32 v209, v209
	v_pk_add_f32 v[202:203], v[202:203], v[248:249] op_sel:[0,0] op_sel_hi:[1,0]
	v_pk_add_f32 v[204:205], v[204:205], v[248:249] op_sel:[0,0] op_sel_hi:[1,0]
	v_pk_add_f32 v[206:207], v[206:207], v[248:249] op_sel:[0,0] op_sel_hi:[1,0]
	v_pk_add_f32 v[208:209], v[208:209], v[248:249] op_sel:[0,0] op_sel_hi:[1,0]
	v_rcp_f32_e32 v202, v202
	v_rcp_f32_e32 v203, v203
	v_rcp_f32_e32 v204, v204
	v_rcp_f32_e32 v205, v205
	v_rcp_f32_e32 v206, v206
	v_rcp_f32_e32 v207, v207
	v_rcp_f32_e32 v208, v208
	v_rcp_f32_e32 v209, v209
	s_waitcnt vmcnt(15)
	v_lshlrev_b32_e32 v242, 16, v186
	v_and_b32_e32 v243, s22, v186
	v_lshlrev_b32_e32 v244, 16, v187
	v_and_b32_e32 v245, s22, v187
	global_load_dwordx2 v[186:187], v234, s[46:47] offset:0
	v_pk_mul_f32 v[210:211], v[202:203], v[88:89] op_sel:[0,0] op_sel_hi:[1,1]
	v_pk_mul_f32 v[212:213], v[204:205], v[90:91] op_sel:[0,0] op_sel_hi:[1,1]
	v_pk_mul_f32 v[206:207], v[206:207], v[242:243] op_sel:[0,0] op_sel_hi:[1,1]
	v_pk_mul_f32 v[208:209], v[208:209], v[244:245] op_sel:[0,0] op_sel_hi:[1,1]
	v_pk_mul_f32 v[214:215], v[210:211], v[246:247] op_sel:[0,1] op_sel_hi:[1,1]
	v_pk_mul_f32 v[216:217], v[212:213], v[246:247] op_sel:[0,1] op_sel_hi:[1,1]
	v_pk_add_f32 v[210:211], v[210:211], v[210:211] op_sel:[0,0] op_sel_hi:[1,1]
	v_pk_add_f32 v[212:213], v[212:213], v[212:213] op_sel:[0,0] op_sel_hi:[1,1]
	v_exp_f32_e32 v214, v214
	v_exp_f32_e32 v215, v215
	v_exp_f32_e32 v216, v216
	v_exp_f32_e32 v217, v217
	v_pk_fma_f32 v[238:239], v[210:211], v[248:249], v[250:251] op_sel:[0,1,0] op_sel_hi:[1,1,0]
	v_pk_fma_f32 v[240:241], v[212:213], v[248:249], v[250:251] op_sel:[0,1,0] op_sel_hi:[1,1,0]
	v_pk_fma_f32 v[238:239], v[210:211], v[238:239], v[250:251] op_sel:[0,0,1] op_sel_hi:[1,1,1]
	v_pk_fma_f32 v[240:241], v[212:213], v[240:241], v[250:251] op_sel:[0,0,1] op_sel_hi:[1,1,1]
	v_pk_fma_f32 v[238:239], v[210:211], v[238:239], v[252:253] op_sel:[0,0,0] op_sel_hi:[1,1,0]
	v_pk_fma_f32 v[240:241], v[212:213], v[240:241], v[252:253] op_sel:[0,0,0] op_sel_hi:[1,1,0]
	v_pk_fma_f32 v[238:239], v[210:211], v[238:239], v[248:249] op_sel:[0,0,0] op_sel_hi:[1,1,0]
	v_pk_fma_f32 v[240:241], v[212:213], v[240:241], v[248:249] op_sel:[0,0,0] op_sel_hi:[1,1,0]
	v_pk_mul_f32 v[238:239], v[210:211], v[238:239] op_sel:[0,0] op_sel_hi:[1,1] neg_lo:[1,0] neg_hi:[1,0]
	v_pk_mul_f32 v[240:241], v[212:213], v[240:241] op_sel:[0,0] op_sel_hi:[1,1] neg_lo:[1,0] neg_hi:[1,0]
	v_pk_fma_f32 v[242:243], v[214:215], v[214:215], v[248:249] op_sel:[0,0,0] op_sel_hi:[1,1,0] neg_lo:[1,0,0] neg_hi:[1,0,0]
	v_pk_fma_f32 v[244:245], v[216:217], v[216:217], v[248:249] op_sel:[0,0,0] op_sel_hi:[1,1,0] neg_lo:[1,0,0] neg_hi:[1,0,0]
	v_cmp_lt_f32_e64 s[24:25], v253, v210
	v_cmp_lt_f32_e64 s[26:27], v253, v211
	v_cmp_lt_f32_e64 s[30:31], v253, v212
	v_cmp_lt_f32_e64 s[34:35], v253, v213
	v_cndmask_b32_e64 v238, v242, v238, s[24:25]
	v_cndmask_b32_e64 v239, v243, v239, s[26:27]
	v_cndmask_b32_e64 v240, v244, v240, s[30:31]
	v_cndmask_b32_e64 v241, v245, v241, s[34:35]
	v_sqrt_f32_e32 v238, v238
	v_sqrt_f32_e32 v239, v239
	v_sqrt_f32_e32 v240, v240
	v_sqrt_f32_e32 v241, v241
	v_pk_mul_f32 v[206:207], v[238:239], v[206:207] op_sel:[0,0] op_sel_hi:[1,1]
	v_pk_mul_f32 v[208:209], v[240:241], v[208:209] op_sel:[0,0] op_sel_hi:[1,1]
	v_pk_fma_f32 v[40:41], v[214:215], v[44:45], v[206:207] op_sel:[0,0,0] op_sel_hi:[1,1,1]
	v_pk_fma_f32 v[42:43], v[216:217], v[46:47], v[208:209] op_sel:[0,0,0] op_sel_hi:[1,1,1]
	v_pk_mul_f32 v[60:61], v[64:65], v[214:215] op_sel:[0,0] op_sel_hi:[1,1]
	v_pk_mul_f32 v[62:63], v[66:67], v[216:217] op_sel:[0,0] op_sel_hi:[1,1]
	v_pk_add_f32 v[202:203], v[24:25], v[72:73] op_sel:[0,0] op_sel_hi:[1,1]
	v_pk_add_f32 v[204:205], v[26:27], v[74:75] op_sel:[0,0] op_sel_hi:[1,1]
	v_pk_add_f32 v[206:207], v[8:9], v[104:105] op_sel:[0,0] op_sel_hi:[1,1]
	v_pk_add_f32 v[208:209], v[10:11], v[106:107] op_sel:[0,0] op_sel_hi:[1,1]
	v_pk_mul_f32 v[202:203], v[202:203], v[246:247] op_sel:[0,0] op_sel_hi:[1,0]
	v_pk_mul_f32 v[204:205], v[204:205], v[246:247] op_sel:[0,0] op_sel_hi:[1,0]
	v_pk_mul_f32 v[206:207], v[206:207], v[246:247] op_sel:[0,0] op_sel_hi:[1,0]
	v_pk_mul_f32 v[208:209], v[208:209], v[246:247] op_sel:[0,0] op_sel_hi:[1,0]
	v_exp_f32_e32 v202, v202
	v_exp_f32_e32 v203, v203
	v_exp_f32_e32 v204, v204
	v_exp_f32_e32 v205, v205
	v_exp_f32_e32 v206, v206
	v_exp_f32_e32 v207, v207
	v_exp_f32_e32 v208, v208
	v_exp_f32_e32 v209, v209
	v_pk_add_f32 v[202:203], v[202:203], v[248:249] op_sel:[0,0] op_sel_hi:[1,0]
	v_pk_add_f32 v[204:205], v[204:205], v[248:249] op_sel:[0,0] op_sel_hi:[1,0]
	v_pk_add_f32 v[206:207], v[206:207], v[248:249] op_sel:[0,0] op_sel_hi:[1,0]
	v_pk_add_f32 v[208:209], v[208:209], v[248:249] op_sel:[0,0] op_sel_hi:[1,0]
	v_rcp_f32_e32 v202, v202
	v_rcp_f32_e32 v203, v203
	v_rcp_f32_e32 v204, v204
	v_rcp_f32_e32 v205, v205
	v_rcp_f32_e32 v206, v206
	v_rcp_f32_e32 v207, v207
	v_rcp_f32_e32 v208, v208
	v_rcp_f32_e32 v209, v209
	s_waitcnt vmcnt(15)
; __device__ __forceinline__ float fast_exp(float x) { return __builtin_amdgcn_exp2f(x * 1.4426950408889634f); }
; __device__ __forceinline__ float fast_sigmoid(float x) { return __builtin_amdgcn_rcpf(1.0f + fast_exp(-x)); }
;     __device__ __forceinline__ void operator()(Acc& acc, const Unit& u, int wr, int wc, int fr_, int fq_, LAS unsigned char* le, int wid, int lane, int&) const {
;     ...
;                 for (int n = 0; n < 2; ++n) {
;                     const f32x4 ba = *(const f32x4*)(b_a + ch0 + n * 16), bi = *(const f32x4*)(b_i + ch0 + n * 16), sl = *(const f32x4*)(spl + ch0 + n * 16);
;                     const u32x2 xw = xpre[ai][m][n]; const float xv[4] = {bflo(xw.x), bfhi(xw.x), bflo(xw.y), bfhi(xw.y)};
;                     const f32x4 ra = acc[ai][0][m][n] + ba, ri = acc[ai][1][m][n] + bi;
; #pragma unroll
;                     for (int j = 0; j < 4; ++j) { const float r = fast_sigmoid(ra[j]), ig = fast_sigmoid(ri[j]);
;                         const float la = -8.0f * r * sl[j];
;                         const float a = fast_exp(la); const float x2 = 2.0f * la;
;                         const float ser = -x2 * (1.0f + x2 * (0.5f + x2 * (1.0f / 6.0f + x2 * (1.0f / 24.0f + x2 * (1.0f / 120.0f)))));
;                         const float om = (x2 > -0.3f) ? ser : (1.0f - a * a);
;                         const float uu = __builtin_amdgcn_sqrtf(om) * (ig * xv[j]);
;                         if (m == 0) { acc[ai][0][m][n][j] = a; acc[ai][1][m][n][j] = uu; }
;                         else { acc[ai][1][m][n][j] = a * acc[ai][1][m - 1][n][j] + uu; acc[ai][0][m][n][j] = acc[ai][0][m - 1][n][j] * a; } } } }
;     ...
;         u32x2 gpre[2][4][2];
; #pragma unroll
;         for (int m = 0; m < 4; ++m)
; #pragma unroll
;             for (int n = 0; n < 2; ++n) gpre[0][m][n] = *(const u32x2*)(gg + roff + (size_t)m * DM + n * 16);
	v_lshlrev_b32_e32 v242, 16, v188
	v_and_b32_e32 v243, s22, v188
	v_lshlrev_b32_e32 v244, 16, v189
	v_and_b32_e32 v245, s22, v189
	global_load_dwordx2 v[188:189], v234, s[46:47] offset:32
	v_pk_mul_f32 v[210:211], v[202:203], v[198:199] op_sel:[0,0] op_sel_hi:[1,1]
	v_pk_mul_f32 v[212:213], v[204:205], v[200:201] op_sel:[0,0] op_sel_hi:[1,1]
	v_pk_mul_f32 v[206:207], v[206:207], v[242:243] op_sel:[0,0] op_sel_hi:[1,1]
	v_pk_mul_f32 v[208:209], v[208:209], v[244:245] op_sel:[0,0] op_sel_hi:[1,1]
	v_pk_mul_f32 v[214:215], v[210:211], v[246:247] op_sel:[0,1] op_sel_hi:[1,1]
	v_pk_mul_f32 v[216:217], v[212:213], v[246:247] op_sel:[0,1] op_sel_hi:[1,1]
	v_pk_add_f32 v[210:211], v[210:211], v[210:211] op_sel:[0,0] op_sel_hi:[1,1]
	v_pk_add_f32 v[212:213], v[212:213], v[212:213] op_sel:[0,0] op_sel_hi:[1,1]
	v_exp_f32_e32 v214, v214
	v_exp_f32_e32 v215, v215
	v_exp_f32_e32 v216, v216
	v_exp_f32_e32 v217, v217
	v_pk_fma_f32 v[238:239], v[210:211], v[248:249], v[250:251] op_sel:[0,1,0] op_sel_hi:[1,1,0]
	v_pk_fma_f32 v[240:241], v[212:213], v[248:249], v[250:251] op_sel:[0,1,0] op_sel_hi:[1,1,0]
	v_pk_fma_f32 v[238:239], v[210:211], v[238:239], v[250:251] op_sel:[0,0,1] op_sel_hi:[1,1,1]
	v_pk_fma_f32 v[240:241], v[212:213], v[240:241], v[250:251] op_sel:[0,0,1] op_sel_hi:[1,1,1]
	v_pk_fma_f32 v[238:239], v[210:211], v[238:239], v[252:253] op_sel:[0,0,0] op_sel_hi:[1,1,0]
	v_pk_fma_f32 v[240:241], v[212:213], v[240:241], v[252:253] op_sel:[0,0,0] op_sel_hi:[1,1,0]
	v_pk_fma_f32 v[238:239], v[210:211], v[238:239], v[248:249] op_sel:[0,0,0] op_sel_hi:[1,1,0]
	v_pk_fma_f32 v[240:241], v[212:213], v[240:241], v[248:249] op_sel:[0,0,0] op_sel_hi:[1,1,0]
	v_pk_mul_f32 v[238:239], v[210:211], v[238:239] op_sel:[0,0] op_sel_hi:[1,1] neg_lo:[1,0] neg_hi:[1,0]
	v_pk_mul_f32 v[240:241], v[212:213], v[240:241] op_sel:[0,0] op_sel_hi:[1,1] neg_lo:[1,0] neg_hi:[1,0]
	v_pk_fma_f32 v[242:243], v[214:215], v[214:215], v[248:249] op_sel:[0,0,0] op_sel_hi:[1,1,0] neg_lo:[1,0,0] neg_hi:[1,0,0]
	v_pk_fma_f32 v[244:245], v[216:217], v[216:217], v[248:249] op_sel:[0,0,0] op_sel_hi:[1,1,0] neg_lo:[1,0,0] neg_hi:[1,0,0]
	v_cmp_lt_f32_e64 s[24:25], v253, v210
	v_cmp_lt_f32_e64 s[26:27], v253, v211
	v_cmp_lt_f32_e64 s[30:31], v253, v212
	v_cmp_lt_f32_e64 s[34:35], v253, v213
	v_cndmask_b32_e64 v238, v242, v238, s[24:25]
	v_cndmask_b32_e64 v239, v243, v239, s[26:27]
	v_cndmask_b32_e64 v240, v244, v240, s[30:31]
	v_cndmask_b32_e64 v241, v245, v241, s[34:35]
	v_sqrt_f32_e32 v238, v238
	v_sqrt_f32_e32 v239, v239
	v_sqrt_f32_e32 v240, v240
	v_sqrt_f32_e32 v241, v241
	v_pk_mul_f32 v[206:207], v[238:239], v[206:207] op_sel:[0,0] op_sel_hi:[1,1]
	v_pk_mul_f32 v[208:209], v[240:241], v[208:209] op_sel:[0,0] op_sel_hi:[1,1]
	v_pk_fma_f32 v[8:9], v[214:215], v[12:13], v[206:207] op_sel:[0,0,0] op_sel_hi:[1,1,1]
	v_pk_fma_f32 v[10:11], v[216:217], v[14:15], v[208:209] op_sel:[0,0,0] op_sel_hi:[1,1,1]
	v_pk_mul_f32 v[24:25], v[28:29], v[214:215] op_sel:[0,0] op_sel_hi:[1,1]
	v_pk_mul_f32 v[26:27], v[30:31], v[216:217] op_sel:[0,0] op_sel_hi:[1,1]
	v_pk_add_f32 v[202:203], v[52:53], v[68:69] op_sel:[0,0] op_sel_hi:[1,1]
	v_pk_add_f32 v[204:205], v[54:55], v[70:71] op_sel:[0,0] op_sel_hi:[1,1]
	v_pk_add_f32 v[206:207], v[36:37], v[100:101] op_sel:[0,0] op_sel_hi:[1,1]
	v_pk_add_f32 v[208:209], v[38:39], v[102:103] op_sel:[0,0] op_sel_hi:[1,1]
	v_pk_mul_f32 v[202:203], v[202:203], v[246:247] op_sel:[0,0] op_sel_hi:[1,0]
	v_pk_mul_f32 v[204:205], v[204:205], v[246:247] op_sel:[0,0] op_sel_hi:[1,0]
	v_pk_mul_f32 v[206:207], v[206:207], v[246:247] op_sel:[0,0] op_sel_hi:[1,0]
	v_pk_mul_f32 v[208:209], v[208:209], v[246:247] op_sel:[0,0] op_sel_hi:[1,0]
	v_exp_f32_e32 v202, v202
	v_exp_f32_e32 v203, v203
	v_exp_f32_e32 v204, v204
	v_exp_f32_e32 v205, v205
	v_exp_f32_e32 v206, v206
	v_exp_f32_e32 v207, v207
	v_exp_f32_e32 v208, v208
	v_exp_f32_e32 v209, v209
	v_pk_add_f32 v[202:203], v[202:203], v[248:249] op_sel:[0,0] op_sel_hi:[1,0]
	v_pk_add_f32 v[204:205], v[204:205], v[248:249] op_sel:[0,0] op_sel_hi:[1,0]
	v_pk_add_f32 v[206:207], v[206:207], v[248:249] op_sel:[0,0] op_sel_hi:[1,0]
	v_pk_add_f32 v[208:209], v[208:209], v[248:249] op_sel:[0,0] op_sel_hi:[1,0]
	v_rcp_f32_e32 v202, v202
	v_rcp_f32_e32 v203, v203
	v_rcp_f32_e32 v204, v204
	v_rcp_f32_e32 v205, v205
	v_rcp_f32_e32 v206, v206
	v_rcp_f32_e32 v207, v207
	v_rcp_f32_e32 v208, v208
	v_rcp_f32_e32 v209, v209
	s_waitcnt vmcnt(15)
; __device__ __forceinline__ float fast_exp(float x) { return __builtin_amdgcn_exp2f(x * 1.4426950408889634f); }
; __device__ __forceinline__ float fast_sigmoid(float x) { return __builtin_amdgcn_rcpf(1.0f + fast_exp(-x)); }
;     __device__ __forceinline__ void operator()(Acc& acc, const Unit& u, int wr, int wc, int fr_, int fq_, LAS unsigned char* le, int wid, int lane, int&) const {
;     ...
;                 for (int n = 0; n < 2; ++n) {
;                     const f32x4 ba = *(const f32x4*)(b_a + ch0 + n * 16), bi = *(const f32x4*)(b_i + ch0 + n * 16), sl = *(const f32x4*)(spl + ch0 + n * 16);
;                     const u32x2 xw = xpre[ai][m][n]; const float xv[4] = {bflo(xw.x), bfhi(xw.x), bflo(xw.y), bfhi(xw.y)};
;                     const f32x4 ra = acc[ai][0][m][n] + ba, ri = acc[ai][1][m][n] + bi;
; #pragma unroll
;                     for (int j = 0; j < 4; ++j) { const float r = fast_sigmoid(ra[j]), ig = fast_sigmoid(ri[j]);
;                         const float la = -8.0f * r * sl[j];
;                         const float a = fast_exp(la); const float x2 = 2.0f * la;
;                         const float ser = -x2 * (1.0f + x2 * (0.5f + x2 * (1.0f / 6.0f + x2 * (1.0f / 24.0f + x2 * (1.0f / 120.0f)))));
;                         const float om = (x2 > -0.3f) ? ser : (1.0f - a * a);
;                         const float uu = __builtin_amdgcn_sqrtf(om) * (ig * xv[j]);
;                         if (m == 0) { acc[ai][0][m][n][j] = a; acc[ai][1][m][n][j] = uu; }
;                         else { acc[ai][1][m][n][j] = a * acc[ai][1][m - 1][n][j] + uu; acc[ai][0][m][n][j] = acc[ai][0][m - 1][n][j] * a; } } } }
;     ...
;         u32x2 gpre[2][4][2];
; #pragma unroll
;         for (int m = 0; m < 4; ++m)
; #pragma unroll
;             for (int n = 0; n < 2; ++n) gpre[0][m][n] = *(const u32x2*)(gg + roff + (size_t)m * DM + n * 16);
	v_lshlrev_b32_e32 v242, 16, v190
	v_and_b32_e32 v243, s22, v190
	v_lshlrev_b32_e32 v244, 16, v191
	v_and_b32_e32 v245, s22, v191
	global_load_dwordx2 v[190:191], v235, s[46:47] offset:0
	v_pk_mul_f32 v[210:211], v[202:203], v[88:89] op_sel:[0,0] op_sel_hi:[1,1]
	v_pk_mul_f32 v[212:213], v[204:205], v[90:91] op_sel:[0,0] op_sel_hi:[1,1]
	v_pk_mul_f32 v[206:207], v[206:207], v[242:243] op_sel:[0,0] op_sel_hi:[1,1]
	v_pk_mul_f32 v[208:209], v[208:209], v[244:245] op_sel:[0,0] op_sel_hi:[1,1]
	v_pk_mul_f32 v[214:215], v[210:211], v[246:247] op_sel:[0,1] op_sel_hi:[1,1]
	v_pk_mul_f32 v[216:217], v[212:213], v[246:247] op_sel:[0,1] op_sel_hi:[1,1]
	v_pk_add_f32 v[210:211], v[210:211], v[210:211] op_sel:[0,0] op_sel_hi:[1,1]
	v_pk_add_f32 v[212:213], v[212:213], v[212:213] op_sel:[0,0] op_sel_hi:[1,1]
	v_exp_f32_e32 v214, v214
	v_exp_f32_e32 v215, v215
	v_exp_f32_e32 v216, v216
	v_exp_f32_e32 v217, v217
	v_pk_fma_f32 v[238:239], v[210:211], v[248:249], v[250:251] op_sel:[0,1,0] op_sel_hi:[1,1,0]
	v_pk_fma_f32 v[240:241], v[212:213], v[248:249], v[250:251] op_sel:[0,1,0] op_sel_hi:[1,1,0]
	v_pk_fma_f32 v[238:239], v[210:211], v[238:239], v[250:251] op_sel:[0,0,1] op_sel_hi:[1,1,1]
	v_pk_fma_f32 v[240:241], v[212:213], v[240:241], v[250:251] op_sel:[0,0,1] op_sel_hi:[1,1,1]
	v_pk_fma_f32 v[238:239], v[210:211], v[238:239], v[252:253] op_sel:[0,0,0] op_sel_hi:[1,1,0]
	v_pk_fma_f32 v[240:241], v[212:213], v[240:241], v[252:253] op_sel:[0,0,0] op_sel_hi:[1,1,0]
	v_pk_fma_f32 v[238:239], v[210:211], v[238:239], v[248:249] op_sel:[0,0,0] op_sel_hi:[1,1,0]
	v_pk_fma_f32 v[240:241], v[212:213], v[240:241], v[248:249] op_sel:[0,0,0] op_sel_hi:[1,1,0]
	v_pk_mul_f32 v[238:239], v[210:211], v[238:239] op_sel:[0,0] op_sel_hi:[1,1] neg_lo:[1,0] neg_hi:[1,0]
	v_pk_mul_f32 v[240:241], v[212:213], v[240:241] op_sel:[0,0] op_sel_hi:[1,1] neg_lo:[1,0] neg_hi:[1,0]
	v_pk_fma_f32 v[242:243], v[214:215], v[214:215], v[248:249] op_sel:[0,0,0] op_sel_hi:[1,1,0] neg_lo:[1,0,0] neg_hi:[1,0,0]
	v_pk_fma_f32 v[244:245], v[216:217], v[216:217], v[248:249] op_sel:[0,0,0] op_sel_hi:[1,1,0] neg_lo:[1,0,0] neg_hi:[1,0,0]
	v_cmp_lt_f32_e64 s[24:25], v253, v210
	v_cmp_lt_f32_e64 s[26:27], v253, v211
	v_cmp_lt_f32_e64 s[30:31], v253, v212
	v_cmp_lt_f32_e64 s[34:35], v253, v213
	v_cndmask_b32_e64 v238, v242, v238, s[24:25]
	v_cndmask_b32_e64 v239, v243, v239, s[26:27]
	v_cndmask_b32_e64 v240, v244, v240, s[30:31]
	v_cndmask_b32_e64 v241, v245, v241, s[34:35]
	v_sqrt_f32_e32 v238, v238
	v_sqrt_f32_e32 v239, v239
	v_sqrt_f32_e32 v240, v240
	v_sqrt_f32_e32 v241, v241
	v_pk_mul_f32 v[206:207], v[238:239], v[206:207] op_sel:[0,0] op_sel_hi:[1,1]
	v_pk_mul_f32 v[208:209], v[240:241], v[208:209] op_sel:[0,0] op_sel_hi:[1,1]
	v_pk_fma_f32 v[36:37], v[214:215], v[40:41], v[206:207] op_sel:[0,0,0] op_sel_hi:[1,1,1]
	v_pk_fma_f32 v[38:39], v[216:217], v[42:43], v[208:209] op_sel:[0,0,0] op_sel_hi:[1,1,1]
	v_pk_mul_f32 v[52:53], v[60:61], v[214:215] op_sel:[0,0] op_sel_hi:[1,1]
	v_pk_mul_f32 v[54:55], v[62:63], v[216:217] op_sel:[0,0] op_sel_hi:[1,1]
	v_pk_add_f32 v[202:203], v[20:21], v[72:73] op_sel:[0,0] op_sel_hi:[1,1]
	v_pk_add_f32 v[204:205], v[22:23], v[74:75] op_sel:[0,0] op_sel_hi:[1,1]
	v_pk_add_f32 v[206:207], v[4:5], v[104:105] op_sel:[0,0] op_sel_hi:[1,1]
	v_pk_add_f32 v[208:209], v[6:7], v[106:107] op_sel:[0,0] op_sel_hi:[1,1]
	v_pk_mul_f32 v[202:203], v[202:203], v[246:247] op_sel:[0,0] op_sel_hi:[1,0]
	v_pk_mul_f32 v[204:205], v[204:205], v[246:247] op_sel:[0,0] op_sel_hi:[1,0]
	v_pk_mul_f32 v[206:207], v[206:207], v[246:247] op_sel:[0,0] op_sel_hi:[1,0]
	v_pk_mul_f32 v[208:209], v[208:209], v[246:247] op_sel:[0,0] op_sel_hi:[1,0]
	v_exp_f32_e32 v202, v202
	v_exp_f32_e32 v203, v203
	v_exp_f32_e32 v204, v204
	v_exp_f32_e32 v205, v205
	v_exp_f32_e32 v206, v206
	v_exp_f32_e32 v207, v207
	v_exp_f32_e32 v208, v208
	v_exp_f32_e32 v209, v209
	v_pk_add_f32 v[202:203], v[202:203], v[248:249] op_sel:[0,0] op_sel_hi:[1,0]
	v_pk_add_f32 v[204:205], v[204:205], v[248:249] op_sel:[0,0] op_sel_hi:[1,0]
	v_pk_add_f32 v[206:207], v[206:207], v[248:249] op_sel:[0,0] op_sel_hi:[1,0]
	v_pk_add_f32 v[208:209], v[208:209], v[248:249] op_sel:[0,0] op_sel_hi:[1,0]
	v_rcp_f32_e32 v202, v202
	v_rcp_f32_e32 v203, v203
	v_rcp_f32_e32 v204, v204
	v_rcp_f32_e32 v205, v205
	v_rcp_f32_e32 v206, v206
	v_rcp_f32_e32 v207, v207
	v_rcp_f32_e32 v208, v208
	v_rcp_f32_e32 v209, v209
	s_waitcnt vmcnt(15)
; __device__ __forceinline__ float fast_exp(float x) { return __builtin_amdgcn_exp2f(x * 1.4426950408889634f); }
; __device__ __forceinline__ float fast_sigmoid(float x) { return __builtin_amdgcn_rcpf(1.0f + fast_exp(-x)); }
;     __device__ __forceinline__ void operator()(Acc& acc, const Unit& u, int wr, int wc, int fr_, int fq_, LAS unsigned char* le, int wid, int lane, int&) const {
;     ...
;                 for (int n = 0; n < 2; ++n) {
;                     const f32x4 ba = *(const f32x4*)(b_a + ch0 + n * 16), bi = *(const f32x4*)(b_i + ch0 + n * 16), sl = *(const f32x4*)(spl + ch0 + n * 16);
;                     const u32x2 xw = xpre[ai][m][n]; const float xv[4] = {bflo(xw.x), bfhi(xw.x), bflo(xw.y), bfhi(xw.y)};
;                     const f32x4 ra = acc[ai][0][m][n] + ba, ri = acc[ai][1][m][n] + bi;
; #pragma unroll
;                     for (int j = 0; j < 4; ++j) { const float r = fast_sigmoid(ra[j]), ig = fast_sigmoid(ri[j]);
;                         const float la = -8.0f * r * sl[j];
;                         const float a = fast_exp(la); const float x2 = 2.0f * la;
;                         const float ser = -x2 * (1.0f + x2 * (0.5f + x2 * (1.0f / 6.0f + x2 * (1.0f / 24.0f + x2 * (1.0f / 120.0f)))));
;                         const float om = (x2 > -0.3f) ? ser : (1.0f - a * a);
;                         const float uu = __builtin_amdgcn_sqrtf(om) * (ig * xv[j]);
;                         if (m == 0) { acc[ai][0][m][n][j] = a; acc[ai][1][m][n][j] = uu; }
;                         else { acc[ai][1][m][n][j] = a * acc[ai][1][m - 1][n][j] + uu; acc[ai][0][m][n][j] = acc[ai][0][m - 1][n][j] * a; } } } }
;     ...
;         u32x2 gpre[2][4][2];
; #pragma unroll
;         for (int m = 0; m < 4; ++m)
; #pragma unroll
;             for (int n = 0; n < 2; ++n) gpre[0][m][n] = *(const u32x2*)(gg + roff + (size_t)m * DM + n * 16);
	v_lshlrev_b32_e32 v242, 16, v192
	v_and_b32_e32 v243, s22, v192
	v_lshlrev_b32_e32 v244, 16, v193
	v_and_b32_e32 v245, s22, v193
	global_load_dwordx2 v[192:193], v235, s[46:47] offset:32
	v_pk_mul_f32 v[210:211], v[202:203], v[198:199] op_sel:[0,0] op_sel_hi:[1,1]
	v_pk_mul_f32 v[212:213], v[204:205], v[200:201] op_sel:[0,0] op_sel_hi:[1,1]
	v_pk_mul_f32 v[206:207], v[206:207], v[242:243] op_sel:[0,0] op_sel_hi:[1,1]
	v_pk_mul_f32 v[208:209], v[208:209], v[244:245] op_sel:[0,0] op_sel_hi:[1,1]
	v_pk_mul_f32 v[214:215], v[210:211], v[246:247] op_sel:[0,1] op_sel_hi:[1,1]
	v_pk_mul_f32 v[216:217], v[212:213], v[246:247] op_sel:[0,1] op_sel_hi:[1,1]
	v_pk_add_f32 v[210:211], v[210:211], v[210:211] op_sel:[0,0] op_sel_hi:[1,1]
	v_pk_add_f32 v[212:213], v[212:213], v[212:213] op_sel:[0,0] op_sel_hi:[1,1]
	v_exp_f32_e32 v214, v214
	v_exp_f32_e32 v215, v215
	v_exp_f32_e32 v216, v216
	v_exp_f32_e32 v217, v217
	v_pk_fma_f32 v[238:239], v[210:211], v[248:249], v[250:251] op_sel:[0,1,0] op_sel_hi:[1,1,0]
	v_pk_fma_f32 v[240:241], v[212:213], v[248:249], v[250:251] op_sel:[0,1,0] op_sel_hi:[1,1,0]
	v_pk_fma_f32 v[238:239], v[210:211], v[238:239], v[250:251] op_sel:[0,0,1] op_sel_hi:[1,1,1]
	v_pk_fma_f32 v[240:241], v[212:213], v[240:241], v[250:251] op_sel:[0,0,1] op_sel_hi:[1,1,1]
	v_pk_fma_f32 v[238:239], v[210:211], v[238:239], v[252:253] op_sel:[0,0,0] op_sel_hi:[1,1,0]
	v_pk_fma_f32 v[240:241], v[212:213], v[240:241], v[252:253] op_sel:[0,0,0] op_sel_hi:[1,1,0]
	v_pk_fma_f32 v[238:239], v[210:211], v[238:239], v[248:249] op_sel:[0,0,0] op_sel_hi:[1,1,0]
	v_pk_fma_f32 v[240:241], v[212:213], v[240:241], v[248:249] op_sel:[0,0,0] op_sel_hi:[1,1,0]
	v_pk_mul_f32 v[238:239], v[210:211], v[238:239] op_sel:[0,0] op_sel_hi:[1,1] neg_lo:[1,0] neg_hi:[1,0]
	v_pk_mul_f32 v[240:241], v[212:213], v[240:241] op_sel:[0,0] op_sel_hi:[1,1] neg_lo:[1,0] neg_hi:[1,0]
	v_pk_fma_f32 v[242:243], v[214:215], v[214:215], v[248:249] op_sel:[0,0,0] op_sel_hi:[1,1,0] neg_lo:[1,0,0] neg_hi:[1,0,0]
	v_pk_fma_f32 v[244:245], v[216:217], v[216:217], v[248:249] op_sel:[0,0,0] op_sel_hi:[1,1,0] neg_lo:[1,0,0] neg_hi:[1,0,0]
	v_cmp_lt_f32_e64 s[24:25], v253, v210
	v_cmp_lt_f32_e64 s[26:27], v253, v211
	v_cmp_lt_f32_e64 s[30:31], v253, v212
	v_cmp_lt_f32_e64 s[34:35], v253, v213
	v_cndmask_b32_e64 v238, v242, v238, s[24:25]
	v_cndmask_b32_e64 v239, v243, v239, s[26:27]
	v_cndmask_b32_e64 v240, v244, v240, s[30:31]
	v_cndmask_b32_e64 v241, v245, v241, s[34:35]
	v_sqrt_f32_e32 v238, v238
	v_sqrt_f32_e32 v239, v239
	v_sqrt_f32_e32 v240, v240
	v_sqrt_f32_e32 v241, v241
	v_pk_mul_f32 v[206:207], v[238:239], v[206:207] op_sel:[0,0] op_sel_hi:[1,1]
	v_pk_mul_f32 v[208:209], v[240:241], v[208:209] op_sel:[0,0] op_sel_hi:[1,1]
	v_pk_fma_f32 v[4:5], v[214:215], v[8:9], v[206:207] op_sel:[0,0,0] op_sel_hi:[1,1,1]
	v_pk_fma_f32 v[6:7], v[216:217], v[10:11], v[208:209] op_sel:[0,0,0] op_sel_hi:[1,1,1]
	v_pk_mul_f32 v[20:21], v[24:25], v[214:215] op_sel:[0,0] op_sel_hi:[1,1]
	v_pk_mul_f32 v[22:23], v[26:27], v[216:217] op_sel:[0,0] op_sel_hi:[1,1]
	v_pk_add_f32 v[202:203], v[48:49], v[68:69] op_sel:[0,0] op_sel_hi:[1,1]
	v_pk_add_f32 v[204:205], v[50:51], v[70:71] op_sel:[0,0] op_sel_hi:[1,1]
	v_pk_add_f32 v[206:207], v[32:33], v[100:101] op_sel:[0,0] op_sel_hi:[1,1]
	v_pk_add_f32 v[208:209], v[34:35], v[102:103] op_sel:[0,0] op_sel_hi:[1,1]
	v_pk_mul_f32 v[202:203], v[202:203], v[246:247] op_sel:[0,0] op_sel_hi:[1,0]
	v_pk_mul_f32 v[204:205], v[204:205], v[246:247] op_sel:[0,0] op_sel_hi:[1,0]
	v_pk_mul_f32 v[206:207], v[206:207], v[246:247] op_sel:[0,0] op_sel_hi:[1,0]
	v_pk_mul_f32 v[208:209], v[208:209], v[246:247] op_sel:[0,0] op_sel_hi:[1,0]
	v_exp_f32_e32 v202, v202
	v_exp_f32_e32 v203, v203
	v_exp_f32_e32 v204, v204
	v_exp_f32_e32 v205, v205
	v_exp_f32_e32 v206, v206
	v_exp_f32_e32 v207, v207
	v_exp_f32_e32 v208, v208
	v_exp_f32_e32 v209, v209
	v_pk_add_f32 v[202:203], v[202:203], v[248:249] op_sel:[0,0] op_sel_hi:[1,0]
	v_pk_add_f32 v[204:205], v[204:205], v[248:249] op_sel:[0,0] op_sel_hi:[1,0]
	v_pk_add_f32 v[206:207], v[206:207], v[248:249] op_sel:[0,0] op_sel_hi:[1,0]
	v_pk_add_f32 v[208:209], v[208:209], v[248:249] op_sel:[0,0] op_sel_hi:[1,0]
	v_rcp_f32_e32 v202, v202
	v_rcp_f32_e32 v203, v203
	v_rcp_f32_e32 v204, v204
	v_rcp_f32_e32 v205, v205
	v_rcp_f32_e32 v206, v206
	v_rcp_f32_e32 v207, v207
	v_rcp_f32_e32 v208, v208
	v_rcp_f32_e32 v209, v209
	s_waitcnt vmcnt(15)
; __device__ __forceinline__ float fast_exp(float x) { return __builtin_amdgcn_exp2f(x * 1.4426950408889634f); }
; __device__ __forceinline__ float fast_sigmoid(float x) { return __builtin_amdgcn_rcpf(1.0f + fast_exp(-x)); }
;     __device__ __forceinline__ void operator()(Acc& acc, const Unit& u, int wr, int wc, int fr_, int fq_, LAS unsigned char* le, int wid, int lane, int&) const {
;     ...
;                 for (int n = 0; n < 2; ++n) {
;                     const f32x4 ba = *(const f32x4*)(b_a + ch0 + n * 16), bi = *(const f32x4*)(b_i + ch0 + n * 16), sl = *(const f32x4*)(spl + ch0 + n * 16);
;                     const u32x2 xw = xpre[ai][m][n]; const float xv[4] = {bflo(xw.x), bfhi(xw.x), bflo(xw.y), bfhi(xw.y)};
;                     const f32x4 ra = acc[ai][0][m][n] + ba, ri = acc[ai][1][m][n] + bi;
; #pragma unroll
;                     for (int j = 0; j < 4; ++j) { const float r = fast_sigmoid(ra[j]), ig = fast_sigmoid(ri[j]);
;                         const float la = -8.0f * r * sl[j];
;                         const float a = fast_exp(la); const float x2 = 2.0f * la;
;                         const float ser = -x2 * (1.0f + x2 * (0.5f + x2 * (1.0f / 6.0f + x2 * (1.0f / 24.0f + x2 * (1.0f / 120.0f)))));
;                         const float om = (x2 > -0.3f) ? ser : (1.0f - a * a);
;                         const float uu = __builtin_amdgcn_sqrtf(om) * (ig * xv[j]);
;                         if (m == 0) { acc[ai][0][m][n][j] = a; acc[ai][1][m][n][j] = uu; }
;                         else { acc[ai][1][m][n][j] = a * acc[ai][1][m - 1][n][j] + uu; acc[ai][0][m][n][j] = acc[ai][0][m - 1][n][j] * a; } } } }
;     ...
;         u32x2 gpre[2][4][2];
; #pragma unroll
;         for (int m = 0; m < 4; ++m)
; #pragma unroll
;             for (int n = 0; n < 2; ++n) gpre[0][m][n] = *(const u32x2*)(gg + roff + (size_t)m * DM + n * 16);
	v_lshlrev_b32_e32 v242, 16, v194
	v_and_b32_e32 v243, s22, v194
	v_lshlrev_b32_e32 v244, 16, v195
	v_and_b32_e32 v245, s22, v195
	global_load_dwordx2 v[194:195], v236, s[46:47] offset:0
	v_pk_mul_f32 v[210:211], v[202:203], v[88:89] op_sel:[0,0] op_sel_hi:[1,1]
	v_pk_mul_f32 v[212:213], v[204:205], v[90:91] op_sel:[0,0] op_sel_hi:[1,1]
	v_pk_mul_f32 v[206:207], v[206:207], v[242:243] op_sel:[0,0] op_sel_hi:[1,1]
	v_pk_mul_f32 v[208:209], v[208:209], v[244:245] op_sel:[0,0] op_sel_hi:[1,1]
	v_pk_mul_f32 v[214:215], v[210:211], v[246:247] op_sel:[0,1] op_sel_hi:[1,1]
	v_pk_mul_f32 v[216:217], v[212:213], v[246:247] op_sel:[0,1] op_sel_hi:[1,1]
	v_pk_add_f32 v[210:211], v[210:211], v[210:211] op_sel:[0,0] op_sel_hi:[1,1]
	v_pk_add_f32 v[212:213], v[212:213], v[212:213] op_sel:[0,0] op_sel_hi:[1,1]
	v_exp_f32_e32 v214, v214
	v_exp_f32_e32 v215, v215
	v_exp_f32_e32 v216, v216
	v_exp_f32_e32 v217, v217
	v_pk_fma_f32 v[238:239], v[210:211], v[248:249], v[250:251] op_sel:[0,1,0] op_sel_hi:[1,1,0]
	v_pk_fma_f32 v[240:241], v[212:213], v[248:249], v[250:251] op_sel:[0,1,0] op_sel_hi:[1,1,0]
	v_pk_fma_f32 v[238:239], v[210:211], v[238:239], v[250:251] op_sel:[0,0,1] op_sel_hi:[1,1,1]
	v_pk_fma_f32 v[240:241], v[212:213], v[240:241], v[250:251] op_sel:[0,0,1] op_sel_hi:[1,1,1]
	v_pk_fma_f32 v[238:239], v[210:211], v[238:239], v[252:253] op_sel:[0,0,0] op_sel_hi:[1,1,0]
	v_pk_fma_f32 v[240:241], v[212:213], v[240:241], v[252:253] op_sel:[0,0,0] op_sel_hi:[1,1,0]
	v_pk_fma_f32 v[238:239], v[210:211], v[238:239], v[248:249] op_sel:[0,0,0] op_sel_hi:[1,1,0]
	v_pk_fma_f32 v[240:241], v[212:213], v[240:241], v[248:249] op_sel:[0,0,0] op_sel_hi:[1,1,0]
	v_pk_mul_f32 v[238:239], v[210:211], v[238:239] op_sel:[0,0] op_sel_hi:[1,1] neg_lo:[1,0] neg_hi:[1,0]
	v_pk_mul_f32 v[240:241], v[212:213], v[240:241] op_sel:[0,0] op_sel_hi:[1,1] neg_lo:[1,0] neg_hi:[1,0]
	v_pk_fma_f32 v[242:243], v[214:215], v[214:215], v[248:249] op_sel:[0,0,0] op_sel_hi:[1,1,0] neg_lo:[1,0,0] neg_hi:[1,0,0]
	v_pk_fma_f32 v[244:245], v[216:217], v[216:217], v[248:249] op_sel:[0,0,0] op_sel_hi:[1,1,0] neg_lo:[1,0,0] neg_hi:[1,0,0]
	v_cmp_lt_f32_e64 s[24:25], v253, v210
	v_cmp_lt_f32_e64 s[26:27], v253, v211
	v_cmp_lt_f32_e64 s[30:31], v253, v212
	v_cmp_lt_f32_e64 s[34:35], v253, v213
	v_cndmask_b32_e64 v238, v242, v238, s[24:25]
	v_cndmask_b32_e64 v239, v243, v239, s[26:27]
	v_cndmask_b32_e64 v240, v244, v240, s[30:31]
	v_cndmask_b32_e64 v241, v245, v241, s[34:35]
	v_sqrt_f32_e32 v238, v238
	v_sqrt_f32_e32 v239, v239
	v_sqrt_f32_e32 v240, v240
	v_sqrt_f32_e32 v241, v241
	v_pk_mul_f32 v[206:207], v[238:239], v[206:207] op_sel:[0,0] op_sel_hi:[1,1]
	v_pk_mul_f32 v[208:209], v[240:241], v[208:209] op_sel:[0,0] op_sel_hi:[1,1]
	v_pk_fma_f32 v[32:33], v[214:215], v[36:37], v[206:207] op_sel:[0,0,0] op_sel_hi:[1,1,1]
	v_pk_fma_f32 v[34:35], v[216:217], v[38:39], v[208:209] op_sel:[0,0,0] op_sel_hi:[1,1,1]
	v_pk_mul_f32 v[48:49], v[52:53], v[214:215] op_sel:[0,0] op_sel_hi:[1,1]
	v_pk_mul_f32 v[50:51], v[54:55], v[216:217] op_sel:[0,0] op_sel_hi:[1,1]
	v_pk_add_f32 v[202:203], v[16:17], v[72:73] op_sel:[0,0] op_sel_hi:[1,1]
	v_pk_add_f32 v[204:205], v[18:19], v[74:75] op_sel:[0,0] op_sel_hi:[1,1]
	v_pk_add_f32 v[206:207], v[0:1], v[104:105] op_sel:[0,0] op_sel_hi:[1,1]
	v_pk_add_f32 v[208:209], v[2:3], v[106:107] op_sel:[0,0] op_sel_hi:[1,1]
	v_pk_mul_f32 v[202:203], v[202:203], v[246:247] op_sel:[0,0] op_sel_hi:[1,0]
	v_pk_mul_f32 v[204:205], v[204:205], v[246:247] op_sel:[0,0] op_sel_hi:[1,0]
	v_pk_mul_f32 v[206:207], v[206:207], v[246:247] op_sel:[0,0] op_sel_hi:[1,0]
	v_pk_mul_f32 v[208:209], v[208:209], v[246:247] op_sel:[0,0] op_sel_hi:[1,0]
	v_exp_f32_e32 v202, v202
	v_exp_f32_e32 v203, v203
	v_exp_f32_e32 v204, v204
	v_exp_f32_e32 v205, v205
	v_exp_f32_e32 v206, v206
	v_exp_f32_e32 v207, v207
	v_exp_f32_e32 v208, v208
	v_exp_f32_e32 v209, v209
	v_pk_add_f32 v[202:203], v[202:203], v[248:249] op_sel:[0,0] op_sel_hi:[1,0]
	v_pk_add_f32 v[204:205], v[204:205], v[248:249] op_sel:[0,0] op_sel_hi:[1,0]
	v_pk_add_f32 v[206:207], v[206:207], v[248:249] op_sel:[0,0] op_sel_hi:[1,0]
	v_pk_add_f32 v[208:209], v[208:209], v[248:249] op_sel:[0,0] op_sel_hi:[1,0]
	v_rcp_f32_e32 v202, v202
	v_rcp_f32_e32 v203, v203
	v_rcp_f32_e32 v204, v204
	v_rcp_f32_e32 v205, v205
	v_rcp_f32_e32 v206, v206
	v_rcp_f32_e32 v207, v207
	v_rcp_f32_e32 v208, v208
	v_rcp_f32_e32 v209, v209
	s_waitcnt vmcnt(15)
; #define LAS __attribute__((address_space(3)))
; __device__ __forceinline__ float fast_exp(float x) { return __builtin_amdgcn_exp2f(x * 1.4426950408889634f); }
;     __device__ __forceinline__ void operator()(Acc& acc, const Unit& u, int wr, int wc, int fr_, int fq_, LAS unsigned char* le, int wid, int lane, int&) const {
;     ...
;                     for (int j = 0; j < 4; ++j) { const float r = fast_sigmoid(ra[j]), ig = fast_sigmoid(ri[j]);
;                         const float la = -8.0f * r * sl[j];
;                         const float a = fast_exp(la); const float x2 = 2.0f * la;
;                         const float ser = -x2 * (1.0f + x2 * (0.5f + x2 * (1.0f / 6.0f + x2 * (1.0f / 24.0f + x2 * (1.0f / 120.0f)))));
;                         const float om = (x2 > -0.3f) ? ser : (1.0f - a * a);
;                         const float uu = __builtin_amdgcn_sqrtf(om) * (ig * xv[j]);
;                         if (m == 0) { acc[ai][0][m][n][j] = a; acc[ai][1][m][n][j] = uu; }
;                         else { acc[ai][1][m][n][j] = a * acc[ai][1][m - 1][n][j] + uu; acc[ai][0][m][n][j] = acc[ai][0][m - 1][n][j] * a; } } } }
; #pragma unroll
;             for (int n = 0; n < 2; ++n)
; #pragma unroll
;                 for (int j = 0; j < 4; ++j) { float A = acc[ai][0][3][n][j], H = acc[ai][1][3][n][j];
;                     { const float Ap = DPP_SHR_ID(A, 1.0f, 0x111), Hp = DPP_SHR_ID(H, 0.0f, 0x111); H = A * Hp + H; A = Ap * A; }
;                     { const float Ap = DPP_SHR_ID(A, 1.0f, 0x112), Hp = DPP_SHR_ID(H, 0.0f, 0x112); H = A * Hp + H; A = Ap * A; }
;                     { const float Ap = DPP_SHR_ID(A, 1.0f, 0x114), Hp = DPP_SHR_ID(H, 0.0f, 0x114); H = A * Hp + H; A = Ap * A; }
;                     { const float Ap = DPP_SHR_ID(A, 1.0f, 0x118), Hp = DPP_SHR_ID(H, 0.0f, 0x118); H = A * Hp + H; A = Ap * A; }
;                     EA[ai][n][j] = DPP_SHR_ID(A, 1.0f, 0x111); EH[ai][n][j] = DPP_SHR_ID(H, 0.0f, 0x111);
;                     if (fr == 15) { LAS float* xp = X + (((ai * 2 + wr) * 128) + wc * 32 + n * 16 + fq * 4 + j) * 2; xp[0] = A; xp[1] = H; } }
;     ...
;         u32x2 gpre[2][4][2];
; #pragma unroll
;         for (int m = 0; m < 4; ++m)
; #pragma unroll
;             for (int n = 0; n < 2; ++n) gpre[0][m][n] = *(const u32x2*)(gg + roff + (size_t)m * DM + n * 16);
	v_lshlrev_b32_e32 v242, 16, v196
	v_and_b32_e32 v243, s22, v196
	v_lshlrev_b32_e32 v244, 16, v197
	v_and_b32_e32 v245, s22, v197
	global_load_dwordx2 v[196:197], v236, s[46:47] offset:32
	v_pk_mul_f32 v[210:211], v[202:203], v[198:199] op_sel:[0,0] op_sel_hi:[1,1]
	v_pk_mul_f32 v[212:213], v[204:205], v[200:201] op_sel:[0,0] op_sel_hi:[1,1]
	v_pk_mul_f32 v[206:207], v[206:207], v[242:243] op_sel:[0,0] op_sel_hi:[1,1]
	v_pk_mul_f32 v[208:209], v[208:209], v[244:245] op_sel:[0,0] op_sel_hi:[1,1]
	v_pk_mul_f32 v[214:215], v[210:211], v[246:247] op_sel:[0,1] op_sel_hi:[1,1]
	v_pk_mul_f32 v[216:217], v[212:213], v[246:247] op_sel:[0,1] op_sel_hi:[1,1]
	v_pk_add_f32 v[210:211], v[210:211], v[210:211] op_sel:[0,0] op_sel_hi:[1,1]
	v_pk_add_f32 v[212:213], v[212:213], v[212:213] op_sel:[0,0] op_sel_hi:[1,1]
	v_exp_f32_e32 v214, v214
	v_exp_f32_e32 v215, v215
	v_exp_f32_e32 v216, v216
	v_exp_f32_e32 v217, v217
	v_pk_fma_f32 v[238:239], v[210:211], v[248:249], v[250:251] op_sel:[0,1,0] op_sel_hi:[1,1,0]
	v_pk_fma_f32 v[240:241], v[212:213], v[248:249], v[250:251] op_sel:[0,1,0] op_sel_hi:[1,1,0]
	v_pk_fma_f32 v[238:239], v[210:211], v[238:239], v[250:251] op_sel:[0,0,1] op_sel_hi:[1,1,1]
	v_pk_fma_f32 v[240:241], v[212:213], v[240:241], v[250:251] op_sel:[0,0,1] op_sel_hi:[1,1,1]
	v_pk_fma_f32 v[238:239], v[210:211], v[238:239], v[252:253] op_sel:[0,0,0] op_sel_hi:[1,1,0]
	v_pk_fma_f32 v[240:241], v[212:213], v[240:241], v[252:253] op_sel:[0,0,0] op_sel_hi:[1,1,0]
	v_pk_fma_f32 v[238:239], v[210:211], v[238:239], v[248:249] op_sel:[0,0,0] op_sel_hi:[1,1,0]
	v_pk_fma_f32 v[240:241], v[212:213], v[240:241], v[248:249] op_sel:[0,0,0] op_sel_hi:[1,1,0]
	v_pk_mul_f32 v[238:239], v[210:211], v[238:239] op_sel:[0,0] op_sel_hi:[1,1] neg_lo:[1,0] neg_hi:[1,0]
	v_pk_mul_f32 v[240:241], v[212:213], v[240:241] op_sel:[0,0] op_sel_hi:[1,1] neg_lo:[1,0] neg_hi:[1,0]
	v_pk_fma_f32 v[242:243], v[214:215], v[214:215], v[248:249] op_sel:[0,0,0] op_sel_hi:[1,1,0] neg_lo:[1,0,0] neg_hi:[1,0,0]
	v_pk_fma_f32 v[244:245], v[216:217], v[216:217], v[248:249] op_sel:[0,0,0] op_sel_hi:[1,1,0] neg_lo:[1,0,0] neg_hi:[1,0,0]
	v_cmp_lt_f32_e64 s[24:25], v253, v210
	v_cmp_lt_f32_e64 s[26:27], v253, v211
	v_cmp_lt_f32_e64 s[30:31], v253, v212
	v_cmp_lt_f32_e64 s[34:35], v253, v213
	v_cndmask_b32_e64 v238, v242, v238, s[24:25]
	v_cndmask_b32_e64 v239, v243, v239, s[26:27]
	v_cndmask_b32_e64 v240, v244, v240, s[30:31]
	v_cndmask_b32_e64 v241, v245, v241, s[34:35]
	v_sqrt_f32_e32 v238, v238
	v_sqrt_f32_e32 v239, v239
	v_sqrt_f32_e32 v240, v240
	v_sqrt_f32_e32 v241, v241
	v_pk_mul_f32 v[206:207], v[238:239], v[206:207] op_sel:[0,0] op_sel_hi:[1,1]
	v_pk_mul_f32 v[208:209], v[240:241], v[208:209] op_sel:[0,0] op_sel_hi:[1,1]
	v_pk_fma_f32 v[0:1], v[214:215], v[4:5], v[206:207] op_sel:[0,0,0] op_sel_hi:[1,1,1]
	v_pk_fma_f32 v[2:3], v[216:217], v[6:7], v[208:209] op_sel:[0,0,0] op_sel_hi:[1,1,1]
	v_pk_mul_f32 v[16:17], v[20:21], v[214:215] op_sel:[0,0] op_sel_hi:[1,1]
	v_pk_mul_f32 v[18:19], v[22:23], v[216:217] op_sel:[0,0] op_sel_hi:[1,1]
	v_cmp_eq_u32_e64 s[30:31], 15, v227
	s_lshl_b32 s8, s9, 7
	s_lshl_b32 s12, s10, 5
	s_add_i32 s8, s8, s12
	v_lshl_add_u32 v218, v224, 2, s8
	v_lshlrev_b32_e32 v218, 3, v218
	v_add_u32_e32 v218, 0x20000, v218
	v_mov_b32_e32 v202, v136
	v_mov_b32_e32 v203, v120
	v_mov_b32_e32 v204, v137
	v_mov_b32_e32 v205, v121
	v_mov_b32_e32 v206, v138
	v_mov_b32_e32 v207, v122
	v_mov_b32_e32 v208, v139
	v_mov_b32_e32 v209, v123
	v_mov_b32_e32 v210, v96
	v_mov_b32_e32 v211, v76
	v_mov_b32_e32 v212, v97
	v_mov_b32_e32 v213, v77
	v_mov_b32_e32 v214, v98
	v_mov_b32_e32 v215, v78
	v_mov_b32_e32 v216, v99
	v_mov_b32_e32 v217, v79
	v_fmac_f32_dpp v203, v203, v202 row_shr:1 row_mask:0xf bank_mask:0xf
	v_fmac_f32_dpp v205, v205, v204 row_shr:1 row_mask:0xf bank_mask:0xf
	v_fmac_f32_dpp v207, v207, v206 row_shr:1 row_mask:0xf bank_mask:0xf
	v_fmac_f32_dpp v209, v209, v208 row_shr:1 row_mask:0xf bank_mask:0xf
	v_fmac_f32_dpp v211, v211, v210 row_shr:1 row_mask:0xf bank_mask:0xf
	v_fmac_f32_dpp v213, v213, v212 row_shr:1 row_mask:0xf bank_mask:0xf
	v_fmac_f32_dpp v215, v215, v214 row_shr:1 row_mask:0xf bank_mask:0xf
	v_fmac_f32_dpp v217, v217, v216 row_shr:1 row_mask:0xf bank_mask:0xf
	v_mul_f32_dpp v202, v202, v202 row_shr:1 row_mask:0xf bank_mask:0xf
	v_mul_f32_dpp v204, v204, v204 row_shr:1 row_mask:0xf bank_mask:0xf
	v_mul_f32_dpp v206, v206, v206 row_shr:1 row_mask:0xf bank_mask:0xf
	v_mul_f32_dpp v208, v208, v208 row_shr:1 row_mask:0xf bank_mask:0xf
	v_mul_f32_dpp v210, v210, v210 row_shr:1 row_mask:0xf bank_mask:0xf
	v_mul_f32_dpp v212, v212, v212 row_shr:1 row_mask:0xf bank_mask:0xf
	v_mul_f32_dpp v214, v214, v214 row_shr:1 row_mask:0xf bank_mask:0xf
	v_mul_f32_dpp v216, v216, v216 row_shr:1 row_mask:0xf bank_mask:0xf
	v_fmac_f32_dpp v203, v203, v202 row_shr:2 row_mask:0xf bank_mask:0xf
	v_fmac_f32_dpp v205, v205, v204 row_shr:2 row_mask:0xf bank_mask:0xf
	v_fmac_f32_dpp v207, v207, v206 row_shr:2 row_mask:0xf bank_mask:0xf
	v_fmac_f32_dpp v209, v209, v208 row_shr:2 row_mask:0xf bank_mask:0xf
	v_fmac_f32_dpp v211, v211, v210 row_shr:2 row_mask:0xf bank_mask:0xf
	v_fmac_f32_dpp v213, v213, v212 row_shr:2 row_mask:0xf bank_mask:0xf
	v_fmac_f32_dpp v215, v215, v214 row_shr:2 row_mask:0xf bank_mask:0xf
	v_fmac_f32_dpp v217, v217, v216 row_shr:2 row_mask:0xf bank_mask:0xf
	v_mul_f32_dpp v202, v202, v202 row_shr:2 row_mask:0xf bank_mask:0xf
	v_mul_f32_dpp v204, v204, v204 row_shr:2 row_mask:0xf bank_mask:0xf
	v_mul_f32_dpp v206, v206, v206 row_shr:2 row_mask:0xf bank_mask:0xf
	v_mul_f32_dpp v208, v208, v208 row_shr:2 row_mask:0xf bank_mask:0xf
; #define LAS __attribute__((address_space(3)))
; #define DPP_SHR_ID(x, idv, ctrl) __builtin_bit_cast(float, __builtin_amdgcn_update_dpp(__builtin_bit_cast(int, (float)(idv)), __builtin_bit_cast(int, (x)), (ctrl), 0xf, 0xf, false))
;     __device__ __forceinline__ void operator()(Acc& acc, const Unit& u, int wr, int wc, int fr_, int fq_, LAS unsigned char* le, int wid, int lane, int&) const {
;     ...
;             for (int n = 0; n < 2; ++n)
; #pragma unroll
;                 for (int j = 0; j < 4; ++j) { float A = acc[ai][0][3][n][j], H = acc[ai][1][3][n][j];
;                     { const float Ap = DPP_SHR_ID(A, 1.0f, 0x111), Hp = DPP_SHR_ID(H, 0.0f, 0x111); H = A * Hp + H; A = Ap * A; }
;                     { const float Ap = DPP_SHR_ID(A, 1.0f, 0x112), Hp = DPP_SHR_ID(H, 0.0f, 0x112); H = A * Hp + H; A = Ap * A; }
;                     { const float Ap = DPP_SHR_ID(A, 1.0f, 0x114), Hp = DPP_SHR_ID(H, 0.0f, 0x114); H = A * Hp + H; A = Ap * A; }
;                     { const float Ap = DPP_SHR_ID(A, 1.0f, 0x118), Hp = DPP_SHR_ID(H, 0.0f, 0x118); H = A * Hp + H; A = Ap * A; }
;                     EA[ai][n][j] = DPP_SHR_ID(A, 1.0f, 0x111); EH[ai][n][j] = DPP_SHR_ID(H, 0.0f, 0x111);
;                     if (fr == 15) { LAS float* xp = X + (((ai * 2 + wr) * 128) + wc * 32 + n * 16 + fq * 4 + j) * 2; xp[0] = A; xp[1] = H; } }
	v_mul_f32_dpp v210, v210, v210 row_shr:2 row_mask:0xf bank_mask:0xf
	v_mul_f32_dpp v212, v212, v212 row_shr:2 row_mask:0xf bank_mask:0xf
	v_mul_f32_dpp v214, v214, v214 row_shr:2 row_mask:0xf bank_mask:0xf
	v_mul_f32_dpp v216, v216, v216 row_shr:2 row_mask:0xf bank_mask:0xf
	v_fmac_f32_dpp v203, v203, v202 row_shr:4 row_mask:0xf bank_mask:0xf
	v_fmac_f32_dpp v205, v205, v204 row_shr:4 row_mask:0xf bank_mask:0xf
	v_fmac_f32_dpp v207, v207, v206 row_shr:4 row_mask:0xf bank_mask:0xf
	v_fmac_f32_dpp v209, v209, v208 row_shr:4 row_mask:0xf bank_mask:0xf
	v_fmac_f32_dpp v211, v211, v210 row_shr:4 row_mask:0xf bank_mask:0xf
	v_fmac_f32_dpp v213, v213, v212 row_shr:4 row_mask:0xf bank_mask:0xf
	v_fmac_f32_dpp v215, v215, v214 row_shr:4 row_mask:0xf bank_mask:0xf
	v_fmac_f32_dpp v217, v217, v216 row_shr:4 row_mask:0xf bank_mask:0xf
	v_mul_f32_dpp v202, v202, v202 row_shr:4 row_mask:0xf bank_mask:0xf
	v_mul_f32_dpp v204, v204, v204 row_shr:4 row_mask:0xf bank_mask:0xf
	v_mul_f32_dpp v206, v206, v206 row_shr:4 row_mask:0xf bank_mask:0xf
	v_mul_f32_dpp v208, v208, v208 row_shr:4 row_mask:0xf bank_mask:0xf
	v_mul_f32_dpp v210, v210, v210 row_shr:4 row_mask:0xf bank_mask:0xf
	v_mul_f32_dpp v212, v212, v212 row_shr:4 row_mask:0xf bank_mask:0xf
	v_mul_f32_dpp v214, v214, v214 row_shr:4 row_mask:0xf bank_mask:0xf
	v_mul_f32_dpp v216, v216, v216 row_shr:4 row_mask:0xf bank_mask:0xf
	v_fmac_f32_dpp v203, v203, v202 row_shr:8 row_mask:0xf bank_mask:0xf
	v_fmac_f32_dpp v205, v205, v204 row_shr:8 row_mask:0xf bank_mask:0xf
	v_fmac_f32_dpp v207, v207, v206 row_shr:8 row_mask:0xf bank_mask:0xf
	v_fmac_f32_dpp v209, v209, v208 row_shr:8 row_mask:0xf bank_mask:0xf
	v_fmac_f32_dpp v211, v211, v210 row_shr:8 row_mask:0xf bank_mask:0xf
	v_fmac_f32_dpp v213, v213, v212 row_shr:8 row_mask:0xf bank_mask:0xf
	v_fmac_f32_dpp v215, v215, v214 row_shr:8 row_mask:0xf bank_mask:0xf
	v_fmac_f32_dpp v217, v217, v216 row_shr:8 row_mask:0xf bank_mask:0xf
	v_mul_f32_dpp v202, v202, v202 row_shr:8 row_mask:0xf bank_mask:0xf
	v_mul_f32_dpp v204, v204, v204 row_shr:8 row_mask:0xf bank_mask:0xf
	v_mul_f32_dpp v206, v206, v206 row_shr:8 row_mask:0xf bank_mask:0xf
	v_mul_f32_dpp v208, v208, v208 row_shr:8 row_mask:0xf bank_mask:0xf
	v_mul_f32_dpp v210, v210, v210 row_shr:8 row_mask:0xf bank_mask:0xf
	v_mul_f32_dpp v212, v212, v212 row_shr:8 row_mask:0xf bank_mask:0xf
	v_mul_f32_dpp v214, v214, v214 row_shr:8 row_mask:0xf bank_mask:0xf
	v_mul_f32_dpp v216, v216, v216 row_shr:8 row_mask:0xf bank_mask:0xf
	v_mov_b32_e32 v238, 1.0
	v_mov_b32_e32 v239, 0
	v_mov_b32_e32 v240, 1.0
	v_mov_b32_e32 v241, 0
	v_mov_b32_e32 v242, 1.0
	v_mov_b32_e32 v243, 0
	v_mov_b32_e32 v244, 1.0
	v_mov_b32_e32 v245, 0
	v_mov_b32_e32 v246, 1.0
	v_mov_b32_e32 v247, 0
	v_mov_b32_e32 v248, 1.0
	v_mov_b32_e32 v249, 0
	v_mov_b32_e32 v250, 1.0
	v_mov_b32_e32 v251, 0
	v_mov_b32_e32 v252, 1.0
	v_mov_b32_e32 v253, 0
	v_mov_b32_dpp v238, v202 row_shr:1 row_mask:0xf bank_mask:0xf
	v_mov_b32_dpp v239, v203 row_shr:1 row_mask:0xf bank_mask:0xf
	v_mov_b32_dpp v240, v204 row_shr:1 row_mask:0xf bank_mask:0xf
	v_mov_b32_dpp v241, v205 row_shr:1 row_mask:0xf bank_mask:0xf
	v_mov_b32_dpp v242, v206 row_shr:1 row_mask:0xf bank_mask:0xf
	v_mov_b32_dpp v243, v207 row_shr:1 row_mask:0xf bank_mask:0xf
	v_mov_b32_dpp v244, v208 row_shr:1 row_mask:0xf bank_mask:0xf
	v_mov_b32_dpp v245, v209 row_shr:1 row_mask:0xf bank_mask:0xf
	v_mov_b32_dpp v246, v210 row_shr:1 row_mask:0xf bank_mask:0xf
	v_mov_b32_dpp v247, v211 row_shr:1 row_mask:0xf bank_mask:0xf
	v_mov_b32_dpp v248, v212 row_shr:1 row_mask:0xf bank_mask:0xf
	v_mov_b32_dpp v249, v213 row_shr:1 row_mask:0xf bank_mask:0xf
	v_mov_b32_dpp v250, v214 row_shr:1 row_mask:0xf bank_mask:0xf
	v_mov_b32_dpp v251, v215 row_shr:1 row_mask:0xf bank_mask:0xf
	v_mov_b32_dpp v252, v216 row_shr:1 row_mask:0xf bank_mask:0xf
	v_mov_b32_dpp v253, v217 row_shr:1 row_mask:0xf bank_mask:0xf
	s_and_saveexec_b64 s[34:35], s[30:31]
	ds_write_b64 v218, v[202:203] offset:0
	ds_write_b64 v218, v[204:205] offset:8
	ds_write_b64 v218, v[206:207] offset:16
	ds_write_b64 v218, v[208:209] offset:24
	ds_write_b64 v218, v[210:211] offset:128
	ds_write_b64 v218, v[212:213] offset:136
	ds_write_b64 v218, v[214:215] offset:144
	ds_write_b64 v218, v[216:217] offset:152
	s_mov_b64 exec, s[34:35]
	v_fmac_f32_e32 v132, v148, v239
	v_fmac_f32_e32 v133, v149, v241
	v_fmac_f32_e32 v134, v150, v243
	v_fmac_f32_e32 v135, v151, v245
	v_mul_f32_e32 v148, v148, v238
	v_mul_f32_e32 v149, v149, v240
	v_mul_f32_e32 v150, v150, v242
	v_mul_f32_e32 v151, v151, v244
	v_fmac_f32_e32 v92, v116, v247
	v_fmac_f32_e32 v93, v117, v249
	v_fmac_f32_e32 v94, v118, v251
	v_fmac_f32_e32 v95, v119, v253
	v_mul_f32_e32 v116, v116, v246
	v_mul_f32_e32 v117, v117, v248
	v_mul_f32_e32 v118, v118, v250
	v_mul_f32_e32 v119, v119, v252
	v_fmac_f32_e32 v128, v144, v239
	v_fmac_f32_e32 v129, v145, v241
	v_fmac_f32_e32 v130, v146, v243
	v_fmac_f32_e32 v131, v147, v245
	v_mul_f32_e32 v144, v144, v238
	v_mul_f32_e32 v145, v145, v240
	v_mul_f32_e32 v146, v146, v242
	v_mul_f32_e32 v147, v147, v244
	v_fmac_f32_e32 v84, v112, v247
	v_fmac_f32_e32 v85, v113, v249
	v_fmac_f32_e32 v86, v114, v251
	v_fmac_f32_e32 v87, v115, v253
	v_mul_f32_e32 v112, v112, v246
	v_mul_f32_e32 v113, v113, v248
	v_mul_f32_e32 v114, v114, v250
	v_mul_f32_e32 v115, v115, v252
	v_fmac_f32_e32 v124, v140, v239
	v_fmac_f32_e32 v125, v141, v241
	v_fmac_f32_e32 v126, v142, v243
	v_fmac_f32_e32 v127, v143, v245
	v_mul_f32_e32 v140, v140, v238
	v_mul_f32_e32 v141, v141, v240
	v_mul_f32_e32 v142, v142, v242
	v_mul_f32_e32 v143, v143, v244
	v_fmac_f32_e32 v80, v108, v247
	v_fmac_f32_e32 v81, v109, v249
; #define LAS __attribute__((address_space(3)))
; #define DPP_SHR_ID(x, idv, ctrl) __builtin_bit_cast(float, __builtin_amdgcn_update_dpp(__builtin_bit_cast(int, (float)(idv)), __builtin_bit_cast(int, (x)), (ctrl), 0xf, 0xf, false))
;     __device__ __forceinline__ void operator()(Acc& acc, const Unit& u, int wr, int wc, int fr_, int fq_, LAS unsigned char* le, int wid, int lane, int&) const {
;     ...
;             for (int n = 0; n < 2; ++n)
; #pragma unroll
;                 for (int j = 0; j < 4; ++j) { float A = acc[ai][0][3][n][j], H = acc[ai][1][3][n][j];
;                     { const float Ap = DPP_SHR_ID(A, 1.0f, 0x111), Hp = DPP_SHR_ID(H, 0.0f, 0x111); H = A * Hp + H; A = Ap * A; }
;                     { const float Ap = DPP_SHR_ID(A, 1.0f, 0x112), Hp = DPP_SHR_ID(H, 0.0f, 0x112); H = A * Hp + H; A = Ap * A; }
;                     { const float Ap = DPP_SHR_ID(A, 1.0f, 0x114), Hp = DPP_SHR_ID(H, 0.0f, 0x114); H = A * Hp + H; A = Ap * A; }
;                     { const float Ap = DPP_SHR_ID(A, 1.0f, 0x118), Hp = DPP_SHR_ID(H, 0.0f, 0x118); H = A * Hp + H; A = Ap * A; }
;                     EA[ai][n][j] = DPP_SHR_ID(A, 1.0f, 0x111); EH[ai][n][j] = DPP_SHR_ID(H, 0.0f, 0x111);
;                     if (fr == 15) { LAS float* xp = X + (((ai * 2 + wr) * 128) + wc * 32 + n * 16 + fq * 4 + j) * 2; xp[0] = A; xp[1] = H; } }
	v_fmac_f32_e32 v82, v110, v251
	v_fmac_f32_e32 v83, v111, v253
	v_mul_f32_e32 v108, v108, v246
	v_mul_f32_e32 v109, v109, v248
	v_mul_f32_e32 v110, v110, v250
	v_mul_f32_e32 v111, v111, v252
	v_fmac_f32_e32 v120, v136, v239
	v_fmac_f32_e32 v121, v137, v241
	v_fmac_f32_e32 v122, v138, v243
	v_fmac_f32_e32 v123, v139, v245
	v_mul_f32_e32 v136, v136, v238
	v_mul_f32_e32 v137, v137, v240
	v_mul_f32_e32 v138, v138, v242
	v_mul_f32_e32 v139, v139, v244
	v_fmac_f32_e32 v76, v96, v247
	v_fmac_f32_e32 v77, v97, v249
	v_fmac_f32_e32 v78, v98, v251
	v_fmac_f32_e32 v79, v99, v253
	v_mul_f32_e32 v96, v96, v246
	v_mul_f32_e32 v97, v97, v248
	v_mul_f32_e32 v98, v98, v250
	v_mul_f32_e32 v99, v99, v252
	v_mov_b32_e32 v202, v48
	v_mov_b32_e32 v203, v32
	v_mov_b32_e32 v204, v49
	v_mov_b32_e32 v205, v33
	v_mov_b32_e32 v206, v50
	v_mov_b32_e32 v207, v34
	v_mov_b32_e32 v208, v51
	v_mov_b32_e32 v209, v35
	v_mov_b32_e32 v210, v16
	v_mov_b32_e32 v211, v0
	v_mov_b32_e32 v212, v17
	v_mov_b32_e32 v213, v1
	v_mov_b32_e32 v214, v18
	v_mov_b32_e32 v215, v2
	v_mov_b32_e32 v216, v19
	v_mov_b32_e32 v217, v3
	v_fmac_f32_dpp v203, v203, v202 row_shr:1 row_mask:0xf bank_mask:0xf
	v_fmac_f32_dpp v205, v205, v204 row_shr:1 row_mask:0xf bank_mask:0xf
	v_fmac_f32_dpp v207, v207, v206 row_shr:1 row_mask:0xf bank_mask:0xf
	v_fmac_f32_dpp v209, v209, v208 row_shr:1 row_mask:0xf bank_mask:0xf
	v_fmac_f32_dpp v211, v211, v210 row_shr:1 row_mask:0xf bank_mask:0xf
	v_fmac_f32_dpp v213, v213, v212 row_shr:1 row_mask:0xf bank_mask:0xf
	v_fmac_f32_dpp v215, v215, v214 row_shr:1 row_mask:0xf bank_mask:0xf
	v_fmac_f32_dpp v217, v217, v216 row_shr:1 row_mask:0xf bank_mask:0xf
	v_mul_f32_dpp v202, v202, v202 row_shr:1 row_mask:0xf bank_mask:0xf
	v_mul_f32_dpp v204, v204, v204 row_shr:1 row_mask:0xf bank_mask:0xf
	v_mul_f32_dpp v206, v206, v206 row_shr:1 row_mask:0xf bank_mask:0xf
	v_mul_f32_dpp v208, v208, v208 row_shr:1 row_mask:0xf bank_mask:0xf
	v_mul_f32_dpp v210, v210, v210 row_shr:1 row_mask:0xf bank_mask:0xf
	v_mul_f32_dpp v212, v212, v212 row_shr:1 row_mask:0xf bank_mask:0xf
	v_mul_f32_dpp v214, v214, v214 row_shr:1 row_mask:0xf bank_mask:0xf
	v_mul_f32_dpp v216, v216, v216 row_shr:1 row_mask:0xf bank_mask:0xf
	v_fmac_f32_dpp v203, v203, v202 row_shr:2 row_mask:0xf bank_mask:0xf
	v_fmac_f32_dpp v205, v205, v204 row_shr:2 row_mask:0xf bank_mask:0xf
	v_fmac_f32_dpp v207, v207, v206 row_shr:2 row_mask:0xf bank_mask:0xf
	v_fmac_f32_dpp v209, v209, v208 row_shr:2 row_mask:0xf bank_mask:0xf
	v_fmac_f32_dpp v211, v211, v210 row_shr:2 row_mask:0xf bank_mask:0xf
	v_fmac_f32_dpp v213, v213, v212 row_shr:2 row_mask:0xf bank_mask:0xf
	v_fmac_f32_dpp v215, v215, v214 row_shr:2 row_mask:0xf bank_mask:0xf
	v_fmac_f32_dpp v217, v217, v216 row_shr:2 row_mask:0xf bank_mask:0xf
	v_mul_f32_dpp v202, v202, v202 row_shr:2 row_mask:0xf bank_mask:0xf
	v_mul_f32_dpp v204, v204, v204 row_shr:2 row_mask:0xf bank_mask:0xf
	v_mul_f32_dpp v206, v206, v206 row_shr:2 row_mask:0xf bank_mask:0xf
	v_mul_f32_dpp v208, v208, v208 row_shr:2 row_mask:0xf bank_mask:0xf
	v_mul_f32_dpp v210, v210, v210 row_shr:2 row_mask:0xf bank_mask:0xf
	v_mul_f32_dpp v212, v212, v212 row_shr:2 row_mask:0xf bank_mask:0xf
	v_mul_f32_dpp v214, v214, v214 row_shr:2 row_mask:0xf bank_mask:0xf
	v_mul_f32_dpp v216, v216, v216 row_shr:2 row_mask:0xf bank_mask:0xf
	v_fmac_f32_dpp v203, v203, v202 row_shr:4 row_mask:0xf bank_mask:0xf
	v_fmac_f32_dpp v205, v205, v204 row_shr:4 row_mask:0xf bank_mask:0xf
	v_fmac_f32_dpp v207, v207, v206 row_shr:4 row_mask:0xf bank_mask:0xf
	v_fmac_f32_dpp v209, v209, v208 row_shr:4 row_mask:0xf bank_mask:0xf
	v_fmac_f32_dpp v211, v211, v210 row_shr:4 row_mask:0xf bank_mask:0xf
	v_fmac_f32_dpp v213, v213, v212 row_shr:4 row_mask:0xf bank_mask:0xf
	v_fmac_f32_dpp v215, v215, v214 row_shr:4 row_mask:0xf bank_mask:0xf
	v_fmac_f32_dpp v217, v217, v216 row_shr:4 row_mask:0xf bank_mask:0xf
	v_mul_f32_dpp v202, v202, v202 row_shr:4 row_mask:0xf bank_mask:0xf
	v_mul_f32_dpp v204, v204, v204 row_shr:4 row_mask:0xf bank_mask:0xf
	v_mul_f32_dpp v206, v206, v206 row_shr:4 row_mask:0xf bank_mask:0xf
	v_mul_f32_dpp v208, v208, v208 row_shr:4 row_mask:0xf bank_mask:0xf
	v_mul_f32_dpp v210, v210, v210 row_shr:4 row_mask:0xf bank_mask:0xf
	v_mul_f32_dpp v212, v212, v212 row_shr:4 row_mask:0xf bank_mask:0xf
	v_mul_f32_dpp v214, v214, v214 row_shr:4 row_mask:0xf bank_mask:0xf
	v_mul_f32_dpp v216, v216, v216 row_shr:4 row_mask:0xf bank_mask:0xf
	v_fmac_f32_dpp v203, v203, v202 row_shr:8 row_mask:0xf bank_mask:0xf
	v_fmac_f32_dpp v205, v205, v204 row_shr:8 row_mask:0xf bank_mask:0xf
	v_fmac_f32_dpp v207, v207, v206 row_shr:8 row_mask:0xf bank_mask:0xf
	v_fmac_f32_dpp v209, v209, v208 row_shr:8 row_mask:0xf bank_mask:0xf
	v_fmac_f32_dpp v211, v211, v210 row_shr:8 row_mask:0xf bank_mask:0xf
	v_fmac_f32_dpp v213, v213, v212 row_shr:8 row_mask:0xf bank_mask:0xf
	v_fmac_f32_dpp v215, v215, v214 row_shr:8 row_mask:0xf bank_mask:0xf
	v_fmac_f32_dpp v217, v217, v216 row_shr:8 row_mask:0xf bank_mask:0xf
	v_mul_f32_dpp v202, v202, v202 row_shr:8 row_mask:0xf bank_mask:0xf
; #define LAS __attribute__((address_space(3)))
; #define EPI_BAR() do { asm volatile("s_waitcnt lgkmcnt(0)" ::: "memory"); __builtin_amdgcn_s_barrier(); asm volatile("" ::: "memory"); } while (0)
; #define DPP_SHR_ID(x, idv, ctrl) __builtin_bit_cast(float, __builtin_amdgcn_update_dpp(__builtin_bit_cast(int, (float)(idv)), __builtin_bit_cast(int, (x)), (ctrl), 0xf, 0xf, false))
;     __device__ __forceinline__ void operator()(Acc& acc, const Unit& u, int wr, int wc, int fr_, int fq_, LAS unsigned char* le, int wid, int lane, int&) const {
;     ...
;             for (int n = 0; n < 2; ++n)
; #pragma unroll
;                 for (int j = 0; j < 4; ++j) { float A = acc[ai][0][3][n][j], H = acc[ai][1][3][n][j];
;                     { const float Ap = DPP_SHR_ID(A, 1.0f, 0x111), Hp = DPP_SHR_ID(H, 0.0f, 0x111); H = A * Hp + H; A = Ap * A; }
;                     { const float Ap = DPP_SHR_ID(A, 1.0f, 0x112), Hp = DPP_SHR_ID(H, 0.0f, 0x112); H = A * Hp + H; A = Ap * A; }
;                     { const float Ap = DPP_SHR_ID(A, 1.0f, 0x114), Hp = DPP_SHR_ID(H, 0.0f, 0x114); H = A * Hp + H; A = Ap * A; }
;                     { const float Ap = DPP_SHR_ID(A, 1.0f, 0x118), Hp = DPP_SHR_ID(H, 0.0f, 0x118); H = A * Hp + H; A = Ap * A; }
;                     EA[ai][n][j] = DPP_SHR_ID(A, 1.0f, 0x111); EH[ai][n][j] = DPP_SHR_ID(H, 0.0f, 0x111);
;                     if (fr == 15) { LAS float* xp = X + (((ai * 2 + wr) * 128) + wc * 32 + n * 16 + fq * 4 + j) * 2; xp[0] = A; xp[1] = H; } }
;         }
;         u32x2 gpre[2][4][2];
; #pragma unroll
;         for (int m = 0; m < 4; ++m)
; #pragma unroll
;             for (int n = 0; n < 2; ++n) gpre[0][m][n] = *(const u32x2*)(gg + roff + (size_t)m * DM + n * 16);
;         EPI_BAR();
;         if (tid < 128) { float TA = 1.f, TH = 0.f;
; #pragma unroll
;             for (int blk = 0; blk < 4; ++blk) { const f32x2 ah = *(const LAS f32x2*)(X + (blk * 128 + tid) * 2); TH = ah.x * TH + ah.y; TA = TA * ah.x; }
;             __hip_atomic_store((unsigned long long*)(agg + ((size_t)u.pm * DM + chb + tid) * 2), __builtin_bit_cast(unsigned long long, (f32x2){TA, TH}), __ATOMIC_RELAXED, __HIP_MEMORY_SCOPE_AGENT);
;             asm volatile("s_waitcnt vmcnt(0)" ::: "memory"); }
	v_mul_f32_dpp v204, v204, v204 row_shr:8 row_mask:0xf bank_mask:0xf
	v_mul_f32_dpp v206, v206, v206 row_shr:8 row_mask:0xf bank_mask:0xf
	v_mul_f32_dpp v208, v208, v208 row_shr:8 row_mask:0xf bank_mask:0xf
	v_mul_f32_dpp v210, v210, v210 row_shr:8 row_mask:0xf bank_mask:0xf
	v_mul_f32_dpp v212, v212, v212 row_shr:8 row_mask:0xf bank_mask:0xf
	v_mul_f32_dpp v214, v214, v214 row_shr:8 row_mask:0xf bank_mask:0xf
	v_mul_f32_dpp v216, v216, v216 row_shr:8 row_mask:0xf bank_mask:0xf
	v_mov_b32_e32 v238, 1.0
	v_mov_b32_e32 v239, 0
	v_mov_b32_e32 v240, 1.0
	v_mov_b32_e32 v241, 0
	v_mov_b32_e32 v242, 1.0
	v_mov_b32_e32 v243, 0
	v_mov_b32_e32 v244, 1.0
	v_mov_b32_e32 v245, 0
	v_mov_b32_e32 v246, 1.0
	v_mov_b32_e32 v247, 0
	v_mov_b32_e32 v248, 1.0
	v_mov_b32_e32 v249, 0
	v_mov_b32_e32 v250, 1.0
	v_mov_b32_e32 v251, 0
	v_mov_b32_e32 v252, 1.0
	v_mov_b32_e32 v253, 0
	v_mov_b32_dpp v238, v202 row_shr:1 row_mask:0xf bank_mask:0xf
	v_mov_b32_dpp v239, v203 row_shr:1 row_mask:0xf bank_mask:0xf
	v_mov_b32_dpp v240, v204 row_shr:1 row_mask:0xf bank_mask:0xf
	v_mov_b32_dpp v241, v205 row_shr:1 row_mask:0xf bank_mask:0xf
	v_mov_b32_dpp v242, v206 row_shr:1 row_mask:0xf bank_mask:0xf
	v_mov_b32_dpp v243, v207 row_shr:1 row_mask:0xf bank_mask:0xf
	v_mov_b32_dpp v244, v208 row_shr:1 row_mask:0xf bank_mask:0xf
	v_mov_b32_dpp v245, v209 row_shr:1 row_mask:0xf bank_mask:0xf
	v_mov_b32_dpp v246, v210 row_shr:1 row_mask:0xf bank_mask:0xf
	v_mov_b32_dpp v247, v211 row_shr:1 row_mask:0xf bank_mask:0xf
	v_mov_b32_dpp v248, v212 row_shr:1 row_mask:0xf bank_mask:0xf
	v_mov_b32_dpp v249, v213 row_shr:1 row_mask:0xf bank_mask:0xf
	v_mov_b32_dpp v250, v214 row_shr:1 row_mask:0xf bank_mask:0xf
	v_mov_b32_dpp v251, v215 row_shr:1 row_mask:0xf bank_mask:0xf
	v_mov_b32_dpp v252, v216 row_shr:1 row_mask:0xf bank_mask:0xf
	v_mov_b32_dpp v253, v217 row_shr:1 row_mask:0xf bank_mask:0xf
	s_and_saveexec_b64 s[34:35], s[30:31]
	ds_write_b64 v218, v[202:203] offset:2048
	ds_write_b64 v218, v[204:205] offset:2056
	ds_write_b64 v218, v[206:207] offset:2064
	ds_write_b64 v218, v[208:209] offset:2072
	ds_write_b64 v218, v[210:211] offset:2176
	ds_write_b64 v218, v[212:213] offset:2184
	ds_write_b64 v218, v[214:215] offset:2192
	ds_write_b64 v218, v[216:217] offset:2200
	s_mov_b64 exec, s[34:35]
	v_fmac_f32_e32 v44, v64, v239
	v_fmac_f32_e32 v45, v65, v241
	v_fmac_f32_e32 v46, v66, v243
	v_fmac_f32_e32 v47, v67, v245
	v_mul_f32_e32 v64, v64, v238
	v_mul_f32_e32 v65, v65, v240
	v_mul_f32_e32 v66, v66, v242
	v_mul_f32_e32 v67, v67, v244
	v_fmac_f32_e32 v12, v28, v247
	v_fmac_f32_e32 v13, v29, v249
	v_fmac_f32_e32 v14, v30, v251
	v_fmac_f32_e32 v15, v31, v253
	v_mul_f32_e32 v28, v28, v246
	v_mul_f32_e32 v29, v29, v248
	v_mul_f32_e32 v30, v30, v250
	v_mul_f32_e32 v31, v31, v252
	v_fmac_f32_e32 v40, v60, v239
	v_fmac_f32_e32 v41, v61, v241
	v_fmac_f32_e32 v42, v62, v243
	v_fmac_f32_e32 v43, v63, v245
	v_mul_f32_e32 v60, v60, v238
	v_mul_f32_e32 v61, v61, v240
	v_mul_f32_e32 v62, v62, v242
	v_mul_f32_e32 v63, v63, v244
	v_fmac_f32_e32 v8, v24, v247
	v_fmac_f32_e32 v9, v25, v249
	v_fmac_f32_e32 v10, v26, v251
	v_fmac_f32_e32 v11, v27, v253
	v_mul_f32_e32 v24, v24, v246
	v_mul_f32_e32 v25, v25, v248
	v_mul_f32_e32 v26, v26, v250
	v_mul_f32_e32 v27, v27, v252
	v_fmac_f32_e32 v36, v52, v239
	v_fmac_f32_e32 v37, v53, v241
	v_fmac_f32_e32 v38, v54, v243
	v_fmac_f32_e32 v39, v55, v245
	v_mul_f32_e32 v52, v52, v238
	v_mul_f32_e32 v53, v53, v240
	v_mul_f32_e32 v54, v54, v242
	v_mul_f32_e32 v55, v55, v244
	v_fmac_f32_e32 v4, v20, v247
	v_fmac_f32_e32 v5, v21, v249
	v_fmac_f32_e32 v6, v22, v251
	v_fmac_f32_e32 v7, v23, v253
	v_mul_f32_e32 v20, v20, v246
	v_mul_f32_e32 v21, v21, v248
	v_mul_f32_e32 v22, v22, v250
	v_mul_f32_e32 v23, v23, v252
	v_fmac_f32_e32 v32, v48, v239
	v_fmac_f32_e32 v33, v49, v241
	v_fmac_f32_e32 v34, v50, v243
	v_fmac_f32_e32 v35, v51, v245
	v_mul_f32_e32 v48, v48, v238
	v_mul_f32_e32 v49, v49, v240
	v_mul_f32_e32 v50, v50, v242
	v_mul_f32_e32 v51, v51, v244
	v_fmac_f32_e32 v0, v16, v247
	v_fmac_f32_e32 v1, v17, v249
	v_fmac_f32_e32 v2, v18, v251
	v_fmac_f32_e32 v3, v19, v253
	v_mul_f32_e32 v16, v16, v246
	v_mul_f32_e32 v17, v17, v248
	v_mul_f32_e32 v18, v18, v250
	v_mul_f32_e32 v19, v19, v252
	s_waitcnt lgkmcnt(0)
	s_barrier
	s_cmp_lt_u32 s91, 0x80
	s_cbranch_scc0 .Lp9_lb_skip1
	v_lshlrev_b32_e32 v202, 3, v228
	v_add_u32_e32 v202, 0x20000, v202
	ds_read_b64 v[204:205], v202 offset:0
	ds_read_b64 v[206:207], v202 offset:1024
	ds_read_b64 v[208:209], v202 offset:2048
	ds_read_b64 v[210:211], v202 offset:3072
	s_lshl_b32 s8, s18, 11
	s_add_i32 s8, s8, s11
	v_add_u32_e32 v203, s8, v228
	v_lshlrev_b32_e32 v203, 3, v203
	s_waitcnt lgkmcnt(0)
	v_mov_b32_e32 v212, v204
	v_mov_b32_e32 v213, v205
	v_fma_f32 v213, v206, v213, v207
	v_mul_f32_e32 v212, v212, v206
	v_fma_f32 v213, v208, v213, v209
	v_mul_f32_e32 v212, v212, v208
	v_fma_f32 v213, v210, v213, v211
	v_mul_f32_e32 v212, v212, v210
	global_store_dwordx2 v203, v[212:213], s[50:51] sc1
	s_waitcnt vmcnt(0)
